# stack23 plus all eight first-batch V transposed reads of step B (and the first four of step A) issued right after the last QK MFMA; waits unchanged
# baseline (speedup 1.0000x reference)
; DI void finishSM(f32x16& p0, f32x16& p1, float alpha, float& l_reg, bf16x8& pa0, bf16x8& pa1, bf16x8& pa2, bf16x8& pa3) {
; #pragma unroll
;     for (int r = 0; r < 16; ++r) p1[r] = __builtin_amdgcn_exp2f(p1[r]);
;     float ps = 0;
; #pragma unroll
;     for (int r = 0; r < 16; ++r) ps += p0[r];
; #pragma unroll
;     for (int r = 0; r < 16; ++r) ps += p1[r];
;     { auto rr = __builtin_amdgcn_permlane32_swap(__float_as_uint(ps), __float_as_uint(ps), false, false); ps = __uint_as_float(rr[0]) + __uint_as_float(rr[1]); }
;     l_reg = l_reg * alpha + ps;
;     ...
;     AT_PK4(p0, 0, pa0); AT_PK4(p0, 8, pa1); AT_PK4(p1, 0, pa2); AT_PK4(p1, 8, pa3);
;     ...
; }
; DI void qkt(f32x16& p0, f32x16& p1, const char* Ks, const bf16x8* qr, const f32x16& negm, int r32, int hi) {
; #pragma unroll
;     for (int d0 = 0; d0 < 4; ++d0) { const int cb = (d0 * 16 + hi * 8) * 2;
;         const bf16x8 b0 = *reinterpret_cast<const bf16x8*>(Ks + AT_KSWZ(r32, cb));
;         const bf16x8 b1 = *reinterpret_cast<const bf16x8*>(Ks + AT_KSWZ(32 + r32, cb));
;         p0 = __builtin_amdgcn_mfma_f32_32x32x16_bf16(b0, qr[d0], d0 == 0 ? negm : p0, 0, 0, 0);
;         p1 = __builtin_amdgcn_mfma_f32_32x32x16_bf16(b1, qr[d0], d0 == 0 ? negm : p1, 0, 0, 0); }
; }
; template <int D0> DI void pv_one(f32x16& od, int vb, bf16x8 pa0, bf16x8 pa1, bf16x8 pa2, bf16x8 pa3) {
;     const s16x4 l0 = tr_read<v_rd_off(D0, 0, 0)>(vb), h0 = tr_read<v_rd_off(D0, 0, 1)>(vb), l1 = tr_read<v_rd_off(D0, 1, 0)>(vb), h1 = tr_read<v_rd_off(D0, 1, 1)>(vb);
;     const s16x4 l2 = tr_read<v_rd_off(D0, 2, 0)>(vb), h2 = tr_read<v_rd_off(D0, 2, 1)>(vb), l3 = tr_read<v_rd_off(D0, 3, 0)>(vb), h3 = tr_read<v_rd_off(D0, 3, 1)>(vb);
;     asm volatile("s_waitcnt lgkmcnt(0)" ::: "memory"); AT_SBAR();
;     ...
;     od = __builtin_amdgcn_mfma_f32_32x32x16_bf16(AT_PK(l0, h0), pa0, od, 0, 0, 0);
;     od = __builtin_amdgcn_mfma_f32_32x32x16_bf16(AT_PK(l1, h1), pa1, od, 0, 0, 0);
;     od = __builtin_amdgcn_mfma_f32_32x32x16_bf16(AT_PK(l2, h2), pa2, od, 0, 0, 0);
;     od = __builtin_amdgcn_mfma_f32_32x32x16_bf16(AT_PK(l3, h3), pa3, od, 0, 0, 0);
;     ...
; }
; DI void pv_all_sm(f32x16* o, int vb, bf16x8 pa0, bf16x8 pa1, bf16x8 pa2, bf16x8 pa3, f32x16& p0, f32x16& p1, float& m_ref, f32x16& negm, float& alpha) {
;     pv_one<0>(o[0], vb, pa0, pa1, pa2, pa3);
;     float pmax = p0[0];
; #pragma unroll
;     for (int r = 1; r < 16; ++r) pmax = fmaxf(pmax, p0[r]);
.LBB4_702:
	s_lshl_b32 s26, s66, 13
	s_add_i32 s26, s26, 0
	v_add_u32_e32 v72, s26, v205
	v_add_u32_e32 v112, s26, v206
	v_add_u32_e32 v180, s26, v207
	s_waitcnt lgkmcnt(1)
	v_mfma_f32_32x32x16_bf16 v[128:143], v[64:67], v[156:159], v[80:95]
	ds_read_b128 v[64:67], v72 offset:49152
	ds_read_b128 v[72:75], v72 offset:53248
	ds_read_b128 v[76:79], v112 offset:49152
	ds_read_b128 v[220:223], v112 offset:53248
	s_add_u32 s74, s46, s28
	s_addc_u32 s75, s47, s29
	s_add_u32 s78, s74, 0x23808000
	s_addc_u32 s79, s75, 0
	s_add_u32 s80, s74, 0x2380a000
	s_add_u32 s76, s46, s30
	s_addc_u32 s77, s47, s31
	s_add_u32 s82, s76, 0x21804000
	s_addc_u32 s83, s77, 0
	s_lshl_b32 s92, s64, 14
	s_add_i32 s92, s92, s94
	s_mov_b32 m0, s92
	s_lshl_b32 s96, s64, 13
	global_load_lds_dwordx4 v249, s[78:79]
	s_addk_i32 s92, 0x400
	s_mov_b32 m0, s92
	s_add_i32 s96, s96, s95
	global_load_lds_dwordx4 v250, s[78:79]
	s_nop 0
	s_mov_b32 m0, s96
	s_nop 0
	global_load_lds_dwordx4 v251, s[82:83]
	v_exp_f32_e32 v186, v97
	v_exp_f32_e32 v213, v98
	v_exp_f32_e32 v214, v99
	v_exp_f32_e32 v219, v100
	v_exp_f32_e32 v228, v101
	s_waitcnt lgkmcnt(4)
	v_mfma_f32_32x32x16_bf16 v[112:127], v[68:71], v[156:159], v[80:95]
	ds_read_b128 v[68:71], v180 offset:49152
	ds_read_b128 v[224:227], v180 offset:53248
	v_exp_f32_e32 v180, v96
	v_cvt_pk_bf16_f32 v96, v216, v218
	v_cvt_pk_bf16_f32 v97, v179, v217
	v_cvt_pk_bf16_f32 v98, v177, v215
	v_cvt_pk_bf16_f32 v99, v176, v178
	s_waitcnt lgkmcnt(4)
	v_mfma_f32_32x32x16_bf16 v[112:127], v[72:75], v[152:155], v[112:127]
	v_add_f32_e32 v75, 0, v216
	v_add_f32_e32 v75, v218, v75
	v_add_f32_e32 v75, v179, v75
	v_add_f32_e32 v75, v217, v75
	v_add_f32_e32 v75, v177, v75
	v_add_f32_e32 v75, v215, v75
	v_add_f32_e32 v75, v176, v75
	v_mfma_f32_32x32x16_bf16 v[128:143], v[64:67], v[152:155], v[128:143]
	v_add_f32_e32 v75, v178, v75
	v_add_f32_e32 v75, v173, v75
	v_add_f32_e32 v75, v175, v75
	v_add_f32_e32 v75, v171, v75
	v_add_f32_e32 v75, v174, v75
	v_add_f32_e32 v75, v169, v75
	v_add_f32_e32 v75, v172, v75
	s_waitcnt lgkmcnt(3)
	v_mfma_f32_32x32x16_bf16 v[128:143], v[76:79], v[148:151], v[128:143]
	v_add_f32_e32 v75, v168, v75
	v_add_f32_e32 v75, v170, v75
	v_add_f32_e32 v75, v180, v75
	v_add_f32_e32 v75, v186, v75
	v_exp_f32_e32 v64, v102
	v_exp_f32_e32 v65, v103
	v_exp_f32_e32 v66, v104
	s_waitcnt lgkmcnt(2)
	v_mfma_f32_32x32x16_bf16 v[112:127], v[220:223], v[148:151], v[112:127]
	v_exp_f32_e32 v67, v105
	v_exp_f32_e32 v105, v106
	v_exp_f32_e32 v106, v107
	v_exp_f32_e32 v107, v108
	v_exp_f32_e32 v72, v109
	v_exp_f32_e32 v73, v110
	v_exp_f32_e32 v74, v111
	s_waitcnt lgkmcnt(1)
	v_mfma_f32_32x32x16_bf16 v[128:143], v[68:71], v[144:147], v[128:143]
	v_add_f32_e32 v68, v213, v75
	v_add_f32_e32 v68, v214, v68
	v_add_f32_e32 v68, v219, v68
	v_add_f32_e32 v68, v228, v68
	v_add_f32_e32 v68, v64, v68
	v_add_f32_e32 v68, v65, v68
	v_add_f32_e32 v68, v66, v68
	v_add_f32_e32 v68, v67, v68
	s_waitcnt lgkmcnt(0)
	v_mfma_f32_32x32x16_bf16 v[112:127], v[224:227], v[144:147], v[112:127]
	v_cvt_pk_bf16_f32 v100, v180, v186
	v_cvt_pk_bf16_f32 v103, v64, v65
	v_cvt_pk_bf16_f32 v104, v66, v67
	s_lshl_b32 s67, s65, 14
	v_add_u32_e32 v186, s67, v253
	ds_read_b64_tr_b16 v[64:65], v186 offset:0
	ds_read_b64_tr_b16 v[66:67], v186 offset:0x100
	v_add_f32_e32 v68, v105, v68
	v_add_f32_e32 v68, v106, v68
	v_add_f32_e32 v68, v107, v68
	v_add_f32_e32 v68, v72, v68
	v_add_f32_e32 v68, v73, v68
	v_add_f32_e32 v183, v74, v68
	ds_read_b64_tr_b16 v[68:69], v186 offset:0x1000
	ds_read_b64_tr_b16 v[70:71], v186 offset:0x1100
	v_cvt_pk_bf16_f32 v108, v173, v175
	v_cvt_pk_bf16_f32 v109, v171, v174
	v_cvt_pk_bf16_f32 v110, v169, v172
	v_cvt_pk_bf16_f32 v111, v168, v170
	v_cvt_pk_bf16_f32 v101, v213, v214
	v_cvt_pk_bf16_f32 v102, v219, v228
	v_cvt_pk_bf16_f32 v105, v105, v106
	v_cvt_pk_bf16_f32 v106, v107, v72
	v_cvt_pk_bf16_f32 v107, v73, v74
	ds_read_b64_tr_b16 v[72:73], v186 offset:0x2000
	ds_read_b64_tr_b16 v[74:75], v186 offset:0x2100
	ds_read_b64_tr_b16 v[76:77], v186 offset:0x3000
	ds_read_b64_tr_b16 v[78:79], v186 offset:0x3100
	s_addc_u32 s81, s75, 0
	s_andn2_b64 vcc, exec, s[2:3]
	s_cbranch_vccnz .LBB4_704
	s_mov_b64 s[2:3], s[8:9]
	global_store_dwordx2 v189, v[184:185], s[2:3] nt
.LBB4_704:
	s_waitcnt lgkmcnt(0)
	v_mfma_f32_32x32x16_bf16 v[32:47], v[64:67], v[96:99], v[32:47]
	v_max_f32_e32 v64, v128, v129
	v_max3_f32 v64, v64, v130, v131
	v_max3_f32 v64, v64, v132, v133
	v_max3_f32 v64, v64, v134, v135
	v_max3_f32 v64, v64, v136, v137
	v_mfma_f32_32x32x16_bf16 v[32:47], v[68:71], v[108:111], v[32:47]
	v_max3_f32 v64, v64, v138, v139
	v_max3_f32 v66, v64, v140, v141
	ds_read_b64_tr_b16 v[64:65], v186 offset:0x200
	v_max3_f32 v180, v66, v142, v143
	ds_read_b64_tr_b16 v[66:67], v186 offset:0x300
	ds_read_b64_tr_b16 v[68:69], v186 offset:0x1200
	ds_read_b64_tr_b16 v[70:71], v186 offset:0x1300
	v_mfma_f32_32x32x16_bf16 v[32:47], v[72:75], v[100:103], v[32:47]
	ds_read_b64_tr_b16 v[72:73], v186 offset:0x2200
	ds_read_b64_tr_b16 v[74:75], v186 offset:0x2300
	ds_read_b64_tr_b16 v[214:215], v186 offset:0x3200
	ds_read_b64_tr_b16 v[216:217], v186 offset:0x3300
	v_mfma_f32_32x32x16_bf16 v[32:47], v[76:79], v[104:107], v[32:47]
	s_waitcnt lgkmcnt(0)
	v_mfma_f32_32x32x16_bf16 v[48:63], v[64:67], v[96:99], v[48:63]
	v_max3_f32 v76, v180, v112, v113
	v_max3_f32 v64, v76, v114, v115
	ds_read_b64_tr_b16 v[66:67], v186 offset:0x400
	v_max3_f32 v64, v64, v116, v117
	v_max3_f32 v64, v64, v118, v119
	v_max3_f32 v64, v64, v120, v121
	v_max3_f32 v64, v64, v122, v123
	v_mfma_f32_32x32x16_bf16 v[48:63], v[68:71], v[108:111], v[48:63]
	ds_read_b64_tr_b16 v[68:69], v186 offset:0x500
	ds_read_b64_tr_b16 v[70:71], v186 offset:0x1400
	v_max3_f32 v64, v64, v124, v125
	v_max3_f32 v64, v64, v126, v127
	v_mov_b32_e32 v65, v64
	s_nop 1
	v_permlane32_swap_b32_e32 v64, v65
	v_mfma_f32_32x32x16_bf16 v[48:63], v[72:75], v[100:103], v[48:63]
	ds_read_b64_tr_b16 v[72:73], v186 offset:0x1500
	ds_read_b64_tr_b16 v[74:75], v186 offset:0x2400
	ds_read_b64_tr_b16 v[76:77], v186 offset:0x2500
	ds_read_b64_tr_b16 v[218:219], v186 offset:0x3400
	ds_read_b64_tr_b16 v[220:221], v186 offset:0x3500
	v_mfma_f32_32x32x16_bf16 v[48:63], v[214:217], v[104:107], v[48:63]
	s_waitcnt lgkmcnt(0)
	v_max_f32_e32 v64, v64, v65
	v_mfma_f32_32x32x16_bf16 v[16:31], v[66:69], v[96:99], v[16:31]
	v_cmp_ge_f32_e32 vcc, s25, v64
	s_cmp_eq_u64 vcc, exec
	v_mfma_f32_32x32x16_bf16 v[16:31], v[70:73], v[108:111], v[16:31]
	v_mfma_f32_32x32x16_bf16 v[16:31], v[74:77], v[100:103], v[16:31]
	v_mfma_f32_32x32x16_bf16 v[16:31], v[218:221], v[104:107], v[16:31]
	s_cbranch_scc0 .LBB4_737
	v_mov_b32_e32 v180, 1.0

; #define AT_SBAR() __builtin_amdgcn_sched_barrier(0)
; template <int OFF> DI s16x4 tr_read(int vb) { s16x4 r; asm volatile("ds_read_b64_tr_b16 %0, %1 offset:%2" : "=&v"(r) : "v"(vb), "i"(OFF) : "memory"); return r; }
; DI void finishSM(f32x16& p0, f32x16& p1, float alpha, float& l_reg, bf16x8& pa0, bf16x8& pa1, bf16x8& pa2, bf16x8& pa3) {
; #pragma unroll
;     for (int r = 0; r < 16; ++r) p1[r] = __builtin_amdgcn_exp2f(p1[r]);
;     float ps = 0;
; #pragma unroll
;     for (int r = 0; r < 16; ++r) ps += p0[r];
; #pragma unroll
;     for (int r = 0; r < 16; ++r) ps += p1[r];
;     { auto rr = __builtin_amdgcn_permlane32_swap(__float_as_uint(ps), __float_as_uint(ps), false, false); ps = __uint_as_float(rr[0]) + __uint_as_float(rr[1]); }
;     l_reg = l_reg * alpha + ps;
;     ...
;     AT_PK4(p0, 0, pa0); AT_PK4(p0, 8, pa1); AT_PK4(p1, 0, pa2); AT_PK4(p1, 8, pa3);
;     ...
; }
; DI void qkt(f32x16& p0, f32x16& p1, const char* Ks, const bf16x8* qr, const f32x16& negm, int r32, int hi) {
; #pragma unroll
;     for (int d0 = 0; d0 < 4; ++d0) { const int cb = (d0 * 16 + hi * 8) * 2;
;         const bf16x8 b0 = *reinterpret_cast<const bf16x8*>(Ks + AT_KSWZ(r32, cb));
;         const bf16x8 b1 = *reinterpret_cast<const bf16x8*>(Ks + AT_KSWZ(32 + r32, cb));
;         p0 = __builtin_amdgcn_mfma_f32_32x32x16_bf16(b0, qr[d0], d0 == 0 ? negm : p0, 0, 0, 0);
;         p1 = __builtin_amdgcn_mfma_f32_32x32x16_bf16(b1, qr[d0], d0 == 0 ? negm : p1, 0, 0, 0); }
; }
; template <int D0> DI void pv_one(f32x16& od, int vb, bf16x8 pa0, bf16x8 pa1, bf16x8 pa2, bf16x8 pa3) {
;     const s16x4 l0 = tr_read<v_rd_off(D0, 0, 0)>(vb), h0 = tr_read<v_rd_off(D0, 0, 1)>(vb), l1 = tr_read<v_rd_off(D0, 1, 0)>(vb), h1 = tr_read<v_rd_off(D0, 1, 1)>(vb);
;     const s16x4 l2 = tr_read<v_rd_off(D0, 2, 0)>(vb), h2 = tr_read<v_rd_off(D0, 2, 1)>(vb), l3 = tr_read<v_rd_off(D0, 3, 0)>(vb), h3 = tr_read<v_rd_off(D0, 3, 1)>(vb);
;     asm volatile("s_waitcnt lgkmcnt(0)" ::: "memory"); AT_SBAR();
;     ...
;     od = __builtin_amdgcn_mfma_f32_32x32x16_bf16(AT_PK(l0, h0), pa0, od, 0, 0, 0);
;     od = __builtin_amdgcn_mfma_f32_32x32x16_bf16(AT_PK(l1, h1), pa1, od, 0, 0, 0);
;     od = __builtin_amdgcn_mfma_f32_32x32x16_bf16(AT_PK(l2, h2), pa2, od, 0, 0, 0);
;     od = __builtin_amdgcn_mfma_f32_32x32x16_bf16(AT_PK(l3, h3), pa3, od, 0, 0, 0);
;     ...
; }
.LBB4_723:
	v_exp_f32_e32 v186, v128
	v_exp_f32_e32 v230, v129
	v_exp_f32_e32 v231, v130
	v_exp_f32_e32 v232, v131
	v_exp_f32_e32 v233, v132
	v_exp_f32_e32 v234, v133
	v_exp_f32_e32 v235, v134
	v_exp_f32_e32 v236, v135
	v_exp_f32_e32 v237, v136
	v_exp_f32_e32 v238, v137
	v_exp_f32_e32 v239, v138
	v_exp_f32_e32 v240, v139
	v_exp_f32_e32 v241, v140
	v_exp_f32_e32 v242, v141
	v_exp_f32_e32 v243, v142
	v_exp_f32_e32 v244, v143
	v_add_u32_e32 v101, s78, v205
	v_add_u32_e32 v102, s78, v206
	v_add_u32_e32 v103, s78, v207
	ds_read_b128 v[172:175], v101 offset:49152
	ds_read_b128 v[176:179], v101 offset:53248
	ds_read_b128 v[214:217], v102 offset:49152
	ds_read_b128 v[218:221], v102 offset:53248
	ds_read_b128 v[222:225], v103 offset:49152
	ds_read_b128 v[226:229], v103 offset:53248
	v_exp_f32_e32 v112, v112
	v_exp_f32_e32 v113, v113
	v_exp_f32_e32 v114, v114
	s_waitcnt lgkmcnt(7)
	v_mfma_f32_32x32x16_bf16 v[128:143], v[96:99], v[156:159], v[80:95]
	s_add_u32 s78, s74, 0x2380c000
	s_addc_u32 s79, s75, 0
	s_add_u32 s74, s74, 0x2380e000
	s_addc_u32 s75, s75, 0
	s_add_u32 s76, s76, 0x21806000
	s_addc_u32 s77, s77, 0
	s_lshl_b32 s92, s65, 14
	s_add_i32 s92, s92, s94
	s_mov_b32 m0, s92
	s_lshl_b32 s96, s65, 13
	global_load_lds_dwordx4 v249, s[78:79]
	s_addk_i32 s92, 0x400
	s_mov_b32 m0, s92
	s_add_i32 s96, s96, s95
	global_load_lds_dwordx4 v250, s[78:79]
	s_nop 0
	s_mov_b32 m0, s96
	s_nop 0
	global_load_lds_dwordx4 v251, s[76:77]
	s_nop 0
	v_exp_f32_e32 v115, v115
	v_exp_f32_e32 v116, v116
	v_exp_f32_e32 v117, v117
	v_exp_f32_e32 v118, v118
	v_exp_f32_e32 v119, v119
	s_waitcnt lgkmcnt(6)
	v_mfma_f32_32x32x16_bf16 v[96:111], v[168:171], v[156:159], v[80:95]
	v_exp_f32_e32 v168, v120
	v_add_f32_e32 v120, 0, v186
	v_add_f32_e32 v120, v230, v120
	v_add_f32_e32 v120, v231, v120
	v_add_f32_e32 v120, v232, v120
	v_add_f32_e32 v120, v233, v120
	v_add_f32_e32 v120, v234, v120
	v_add_f32_e32 v120, v235, v120
	v_add_f32_e32 v120, v236, v120
	v_add_f32_e32 v120, v237, v120
	v_add_f32_e32 v120, v238, v120
	s_waitcnt lgkmcnt(5)
	v_mfma_f32_32x32x16_bf16 v[128:143], v[172:175], v[152:155], v[128:143]
	v_add_f32_e32 v120, v239, v120
	v_add_f32_e32 v120, v240, v120
	v_add_f32_e32 v120, v241, v120
	v_add_f32_e32 v120, v242, v120
	v_add_f32_e32 v120, v243, v120
	v_add_f32_e32 v120, v244, v120
	v_add_f32_e32 v120, v112, v120
	s_waitcnt lgkmcnt(4)
	v_mfma_f32_32x32x16_bf16 v[96:111], v[176:179], v[152:155], v[96:111]
	v_add_f32_e32 v120, v113, v120
	v_add_f32_e32 v120, v114, v120
	v_add_f32_e32 v120, v115, v120
	v_add_f32_e32 v120, v116, v120
	v_exp_f32_e32 v169, v121
	v_add_f32_e32 v120, v117, v120
	v_exp_f32_e32 v170, v122
	s_waitcnt lgkmcnt(3)
	v_mfma_f32_32x32x16_bf16 v[128:143], v[214:217], v[148:151], v[128:143]
	v_add_f32_e32 v120, v118, v120
	v_exp_f32_e32 v171, v123
	v_add_f32_e32 v120, v119, v120
	v_exp_f32_e32 v172, v124
	v_add_f32_e32 v120, v168, v120
	v_exp_f32_e32 v173, v125
	v_add_f32_e32 v120, v169, v120
	s_waitcnt lgkmcnt(2)
	v_mfma_f32_32x32x16_bf16 v[96:111], v[218:221], v[148:151], v[96:111]
	v_exp_f32_e32 v174, v126
	v_add_f32_e32 v120, v170, v120
	v_exp_f32_e32 v175, v127
	v_add_f32_e32 v120, v171, v120
	v_add_f32_e32 v120, v172, v120
	v_add_f32_e32 v120, v173, v120
	v_add_f32_e32 v120, v174, v120
	s_waitcnt lgkmcnt(1)
	v_mfma_f32_32x32x16_bf16 v[128:143], v[222:225], v[144:147], v[128:143]
	v_add_f32_e32 v213, v175, v120
	v_cvt_pk_bf16_f32 v120, v186, v230
	v_cvt_pk_bf16_f32 v121, v231, v232
	v_cvt_pk_bf16_f32 v122, v233, v234
	v_cvt_pk_bf16_f32 v123, v235, v236
	v_cvt_pk_bf16_f32 v124, v237, v238
	s_waitcnt lgkmcnt(0)
	v_mfma_f32_32x32x16_bf16 v[96:111], v[226:229], v[144:147], v[96:111]
	v_lshl_add_u32 v215, s66, 14, v253
	ds_read_b64_tr_b16 v[216:217], v215 offset:0
	ds_read_b64_tr_b16 v[218:219], v215 offset:0x100
	ds_read_b64_tr_b16 v[220:221], v215 offset:0x1000
	ds_read_b64_tr_b16 v[222:223], v215 offset:0x1100
	ds_read_b64_tr_b16 v[224:225], v215 offset:0x2000
	ds_read_b64_tr_b16 v[226:227], v215 offset:0x2100
	ds_read_b64_tr_b16 v[228:229], v215 offset:0x3000
	ds_read_b64_tr_b16 v[230:231], v215 offset:0x3100
	v_cvt_pk_bf16_f32 v125, v239, v240
	v_cvt_pk_bf16_f32 v126, v241, v242
	v_cvt_pk_bf16_f32 v127, v243, v244
	v_cvt_pk_bf16_f32 v112, v112, v113
	v_cvt_pk_bf16_f32 v113, v114, v115
	v_cvt_pk_bf16_f32 v114, v116, v117
	v_cvt_pk_bf16_f32 v115, v118, v119
	v_cvt_pk_bf16_f32 v116, v168, v169
	v_cvt_pk_bf16_f32 v117, v170, v171
	v_cvt_pk_bf16_f32 v118, v172, v173
	v_cvt_pk_bf16_f32 v119, v174, v175
	s_and_b64 vcc, exec, s[2:3]
	s_cbranch_vccnz .LBB4_725
	s_mov_b64 s[2:3], s[8:9]
	global_store_dwordx2 v189, v[184:185], s[2:3] nt
; #define AT_SBAR() __builtin_amdgcn_sched_barrier(0)
; template <int OFF> DI s16x4 tr_read(int vb) { s16x4 r; asm volatile("ds_read_b64_tr_b16 %0, %1 offset:%2" : "=&v"(r) : "v"(vb), "i"(OFF) : "memory"); return r; }
; template <int D0> DI void pv_one(f32x16& od, int vb, bf16x8 pa0, bf16x8 pa1, bf16x8 pa2, bf16x8 pa3) {
;     const s16x4 l0 = tr_read<v_rd_off(D0, 0, 0)>(vb), h0 = tr_read<v_rd_off(D0, 0, 1)>(vb), l1 = tr_read<v_rd_off(D0, 1, 0)>(vb), h1 = tr_read<v_rd_off(D0, 1, 1)>(vb);
;     const s16x4 l2 = tr_read<v_rd_off(D0, 2, 0)>(vb), h2 = tr_read<v_rd_off(D0, 2, 1)>(vb), l3 = tr_read<v_rd_off(D0, 3, 0)>(vb), h3 = tr_read<v_rd_off(D0, 3, 1)>(vb);
;     asm volatile("s_waitcnt lgkmcnt(0)" ::: "memory"); AT_SBAR();
;     ...
;     od = __builtin_amdgcn_mfma_f32_32x32x16_bf16(AT_PK(l0, h0), pa0, od, 0, 0, 0);
;     od = __builtin_amdgcn_mfma_f32_32x32x16_bf16(AT_PK(l1, h1), pa1, od, 0, 0, 0);
;     od = __builtin_amdgcn_mfma_f32_32x32x16_bf16(AT_PK(l2, h2), pa2, od, 0, 0, 0);
;     od = __builtin_amdgcn_mfma_f32_32x32x16_bf16(AT_PK(l3, h3), pa3, od, 0, 0, 0);
;     ...
; }
; DI void pv_all_sm(f32x16* o, int vb, bf16x8 pa0, bf16x8 pa1, bf16x8 pa2, bf16x8 pa3, f32x16& p0, f32x16& p1, float& m_ref, f32x16& negm, float& alpha) {
;     pv_one<0>(o[0], vb, pa0, pa1, pa2, pa3);
;     float pmax = p0[0];
; #pragma unroll
;     for (int r = 1; r < 16; ++r) pmax = fmaxf(pmax, p0[r]);
;     pv_one<1>(o[1], vb, pa0, pa1, pa2, pa3);
; #pragma unroll
;     for (int r = 0; r < 16; ++r) pmax = fmaxf(pmax, p1[r]);
;     { auto rr = __builtin_amdgcn_permlane32_swap(__float_as_uint(pmax), __float_as_uint(pmax), false, false); pmax = fmaxf(__uint_as_float(rr[0]), __uint_as_float(rr[1])); }
;     pv_one<2>(o[2], vb, pa0, pa1, pa2, pa3);
;     alpha = 1.f;
;     if (__builtin_expect(!__all(pmax <= THRL), 0)) {
;         const float dl = fmaxf(pmax, 0.f); m_ref += dl; alpha = __builtin_amdgcn_exp2f(-dl);
; #pragma unroll
;         for (int r = 0; r < 16; ++r) { p0[r] -= dl; p1[r] -= dl; }
; #pragma unroll
;         for (int r = 0; r < 16; ++r) negm[r] = -m_ref;
;     }
;     pv_one<3>(o[3], vb, pa0, pa1, pa2, pa3);
; #pragma unroll
;     for (int r = 0; r < 16; ++r) p0[r] = __builtin_amdgcn_exp2f(p0[r]);
; }
.LBB4_725:
	s_waitcnt lgkmcnt(0)
	v_mfma_f32_32x32x16_bf16 v[32:47], v[216:219], v[120:123], v[32:47]
	v_max_f32_e32 v186, v128, v129
	ds_read_b64_tr_b16 v[216:217], v215 offset:0x200
	ds_read_b64_tr_b16 v[218:219], v215 offset:0x300
	v_max3_f32 v186, v186, v130, v131
	v_max3_f32 v186, v186, v132, v133
	v_mfma_f32_32x32x16_bf16 v[32:47], v[220:223], v[124:127], v[32:47]
	ds_read_b64_tr_b16 v[220:221], v215 offset:0x1200
	ds_read_b64_tr_b16 v[222:223], v215 offset:0x1300
	v_max3_f32 v186, v186, v134, v135
	v_max3_f32 v186, v186, v136, v137
	v_max3_f32 v186, v186, v138, v139
	v_max3_f32 v186, v186, v140, v141
	v_max3_f32 v186, v186, v142, v143
	v_mfma_f32_32x32x16_bf16 v[32:47], v[224:227], v[112:115], v[32:47]
	ds_read_b64_tr_b16 v[224:225], v215 offset:0x2200
	ds_read_b64_tr_b16 v[226:227], v215 offset:0x2300
	ds_read_b64_tr_b16 v[232:233], v215 offset:0x3200
	ds_read_b64_tr_b16 v[234:235], v215 offset:0x3300
	v_mfma_f32_32x32x16_bf16 v[32:47], v[228:231], v[116:119], v[32:47]
	s_waitcnt lgkmcnt(0)
	v_mfma_f32_32x32x16_bf16 v[48:63], v[216:219], v[120:123], v[48:63]
	v_max3_f32 v186, v186, v96, v97
	v_max3_f32 v186, v186, v98, v99
	ds_read_b64_tr_b16 v[218:219], v215 offset:0x400
	v_max3_f32 v186, v186, v100, v101
	v_max3_f32 v186, v186, v102, v103
	v_max3_f32 v186, v186, v104, v105
	v_max3_f32 v186, v186, v106, v107
	v_mfma_f32_32x32x16_bf16 v[48:63], v[220:223], v[124:127], v[48:63]
	ds_read_b64_tr_b16 v[220:221], v215 offset:0x500
	ds_read_b64_tr_b16 v[222:223], v215 offset:0x1400
	v_max3_f32 v186, v186, v108, v109
	v_max3_f32 v186, v186, v110, v111
	v_mov_b32_e32 v216, v186
	s_nop 1
	v_permlane32_swap_b32_e32 v186, v216
	v_mfma_f32_32x32x16_bf16 v[48:63], v[224:227], v[112:115], v[48:63]
	ds_read_b64_tr_b16 v[224:225], v215 offset:0x1500
	ds_read_b64_tr_b16 v[226:227], v215 offset:0x2400
	ds_read_b64_tr_b16 v[228:229], v215 offset:0x2500
	ds_read_b64_tr_b16 v[236:237], v215 offset:0x3400
	ds_read_b64_tr_b16 v[238:239], v215 offset:0x3500
	v_mfma_f32_32x32x16_bf16 v[48:63], v[232:235], v[116:119], v[48:63]
	s_waitcnt lgkmcnt(0)
	v_max_f32_e32 v216, v186, v216
	v_mfma_f32_32x32x16_bf16 v[16:31], v[218:221], v[120:123], v[16:31]
	v_cmp_ge_f32_e32 vcc, s25, v216
	s_cmp_eq_u64 vcc, exec
	v_mov_b32_e32 v186, 1.0
	v_mfma_f32_32x32x16_bf16 v[16:31], v[222:225], v[124:127], v[16:31]
	v_mfma_f32_32x32x16_bf16 v[16:31], v[226:229], v[112:115], v[16:31]
	v_mfma_f32_32x32x16_bf16 v[16:31], v[236:239], v[116:119], v[16:31]
	s_cbranch_scc0 .LBB4_738

; DI void finishSM(f32x16& p0, f32x16& p1, float alpha, float& l_reg, bf16x8& pa0, bf16x8& pa1, bf16x8& pa2, bf16x8& pa3) {
; #pragma unroll
;     for (int r = 0; r < 16; ++r) p1[r] = __builtin_amdgcn_exp2f(p1[r]);
;     float ps = 0;
; #pragma unroll
;     for (int r = 0; r < 16; ++r) ps += p0[r];
; #pragma unroll
;     for (int r = 0; r < 16; ++r) ps += p1[r];
;     { auto rr = __builtin_amdgcn_permlane32_swap(__float_as_uint(ps), __float_as_uint(ps), false, false); ps = __uint_as_float(rr[0]) + __uint_as_float(rr[1]); }
;     l_reg = l_reg * alpha + ps;
;     ...
;     AT_PK4(p0, 0, pa0); AT_PK4(p0, 8, pa1); AT_PK4(p1, 0, pa2); AT_PK4(p1, 8, pa3);
;     ...
; }
; DI void qkt(f32x16& p0, f32x16& p1, const char* Ks, const bf16x8* qr, const f32x16& negm, int r32, int hi) {
; #pragma unroll
;     for (int d0 = 0; d0 < 4; ++d0) { const int cb = (d0 * 16 + hi * 8) * 2;
;         const bf16x8 b0 = *reinterpret_cast<const bf16x8*>(Ks + AT_KSWZ(r32, cb));
;         const bf16x8 b1 = *reinterpret_cast<const bf16x8*>(Ks + AT_KSWZ(32 + r32, cb));
;         p0 = __builtin_amdgcn_mfma_f32_32x32x16_bf16(b0, qr[d0], d0 == 0 ? negm : p0, 0, 0, 0);
;         p1 = __builtin_amdgcn_mfma_f32_32x32x16_bf16(b1, qr[d0], d0 == 0 ? negm : p1, 0, 0, 0); }
; }
; template <int D0> DI void pv_one(f32x16& od, int vb, bf16x8 pa0, bf16x8 pa1, bf16x8 pa2, bf16x8 pa3) {
;     const s16x4 l0 = tr_read<v_rd_off(D0, 0, 0)>(vb), h0 = tr_read<v_rd_off(D0, 0, 1)>(vb), l1 = tr_read<v_rd_off(D0, 1, 0)>(vb), h1 = tr_read<v_rd_off(D0, 1, 1)>(vb);
;     const s16x4 l2 = tr_read<v_rd_off(D0, 2, 0)>(vb), h2 = tr_read<v_rd_off(D0, 2, 1)>(vb), l3 = tr_read<v_rd_off(D0, 3, 0)>(vb), h3 = tr_read<v_rd_off(D0, 3, 1)>(vb);
;     asm volatile("s_waitcnt lgkmcnt(0)" ::: "memory"); AT_SBAR();
;     ...
;     od = __builtin_amdgcn_mfma_f32_32x32x16_bf16(AT_PK(l0, h0), pa0, od, 0, 0, 0);
;     od = __builtin_amdgcn_mfma_f32_32x32x16_bf16(AT_PK(l1, h1), pa1, od, 0, 0, 0);
;     od = __builtin_amdgcn_mfma_f32_32x32x16_bf16(AT_PK(l2, h2), pa2, od, 0, 0, 0);
;     od = __builtin_amdgcn_mfma_f32_32x32x16_bf16(AT_PK(l3, h3), pa3, od, 0, 0, 0);
;     ...
; }
; DI void pv_all_sm(f32x16* o, int vb, bf16x8 pa0, bf16x8 pa1, bf16x8 pa2, bf16x8 pa3, f32x16& p0, f32x16& p1, float& m_ref, f32x16& negm, float& alpha) {
;     pv_one<0>(o[0], vb, pa0, pa1, pa2, pa3);
;     float pmax = p0[0];
; #pragma unroll
;     for (int r = 1; r < 16; ++r) pmax = fmaxf(pmax, p0[r]);
.LBB4_775:
	s_lshl_b32 s20, s30, 13
	s_add_i32 s20, s20, 0
	v_add_u32_e32 v72, s20, v208
	v_add_u32_e32 v112, s20, v209
	v_add_u32_e32 v180, s20, v210
	s_waitcnt lgkmcnt(1)
	v_mfma_f32_32x32x16_bf16 v[128:143], v[64:67], v[156:159], v[80:95]
	ds_read_b128 v[64:67], v72 offset:49152
	ds_read_b128 v[72:75], v72 offset:53248
	ds_read_b128 v[76:79], v112 offset:49152
	ds_read_b128 v[224:227], v112 offset:53248
	s_add_u32 s34, s46, s16
	s_addc_u32 s35, s47, s17
	s_add_u32 s24, s34, 0x23808000
	s_addc_u32 s25, s35, 0
	s_add_u32 s66, s34, 0x2380a000
	s_add_u32 s37, s46, s18
	s_addc_u32 s64, s47, s19
	s_add_u32 s74, s37, 0x21884000
	s_addc_u32 s75, s64, 0
	s_lshl_b32 s92, s15, 14
	s_add_i32 s92, s92, s94
	s_mov_b32 m0, s92
	s_lshl_b32 s96, s15, 13
	global_load_lds_dwordx4 v249, s[24:25]
	s_addk_i32 s92, 0x400
	s_mov_b32 m0, s92
	s_add_i32 s96, s96, s95
	global_load_lds_dwordx4 v250, s[24:25]
	s_nop 0
	s_mov_b32 m0, s96
	s_nop 0
	global_load_lds_dwordx4 v251, s[74:75]
	v_exp_f32_e32 v182, v97
	v_exp_f32_e32 v217, v98
	v_exp_f32_e32 v218, v99
	v_exp_f32_e32 v223, v100
	v_exp_f32_e32 v232, v101
	s_waitcnt lgkmcnt(4)
	v_mfma_f32_32x32x16_bf16 v[112:127], v[68:71], v[156:159], v[80:95]
	ds_read_b128 v[68:71], v180 offset:49152
	ds_read_b128 v[228:231], v180 offset:53248
	v_exp_f32_e32 v180, v96
	v_cvt_pk_bf16_f32 v96, v220, v222
	v_cvt_pk_bf16_f32 v97, v179, v221
	v_cvt_pk_bf16_f32 v98, v177, v219
	v_cvt_pk_bf16_f32 v99, v176, v178
	s_waitcnt lgkmcnt(4)
	v_mfma_f32_32x32x16_bf16 v[112:127], v[72:75], v[152:155], v[112:127]
	v_add_f32_e32 v75, 0, v220
	v_add_f32_e32 v75, v222, v75
	v_add_f32_e32 v75, v179, v75
	v_add_f32_e32 v75, v221, v75
	v_add_f32_e32 v75, v177, v75
	v_add_f32_e32 v75, v219, v75
	v_add_f32_e32 v75, v176, v75
	v_mfma_f32_32x32x16_bf16 v[128:143], v[64:67], v[152:155], v[128:143]
	v_add_f32_e32 v75, v178, v75
	v_add_f32_e32 v75, v173, v75
	v_add_f32_e32 v75, v175, v75
	v_add_f32_e32 v75, v171, v75
	v_add_f32_e32 v75, v174, v75
	v_add_f32_e32 v75, v169, v75
	v_add_f32_e32 v75, v172, v75
	s_waitcnt lgkmcnt(3)
	v_mfma_f32_32x32x16_bf16 v[128:143], v[76:79], v[148:151], v[128:143]
	v_add_f32_e32 v75, v168, v75
	v_add_f32_e32 v75, v170, v75
	v_add_f32_e32 v75, v180, v75
	v_add_f32_e32 v75, v182, v75
	v_exp_f32_e32 v64, v102
	v_exp_f32_e32 v65, v103
	v_exp_f32_e32 v66, v104
	s_waitcnt lgkmcnt(2)
	v_mfma_f32_32x32x16_bf16 v[112:127], v[224:227], v[148:151], v[112:127]
	v_exp_f32_e32 v67, v105
	v_exp_f32_e32 v105, v106
	v_exp_f32_e32 v106, v107
	v_exp_f32_e32 v107, v108
	v_exp_f32_e32 v72, v109
	v_exp_f32_e32 v73, v110
	v_exp_f32_e32 v74, v111
	s_waitcnt lgkmcnt(1)
	v_mfma_f32_32x32x16_bf16 v[128:143], v[68:71], v[144:147], v[128:143]
	v_add_f32_e32 v68, v217, v75
	v_add_f32_e32 v68, v218, v68
	v_add_f32_e32 v68, v223, v68
	v_add_f32_e32 v68, v232, v68
	v_add_f32_e32 v68, v64, v68
	v_add_f32_e32 v68, v65, v68
	v_add_f32_e32 v68, v66, v68
	v_add_f32_e32 v68, v67, v68
	s_waitcnt lgkmcnt(0)
	v_mfma_f32_32x32x16_bf16 v[112:127], v[228:231], v[144:147], v[112:127]
	v_cvt_pk_bf16_f32 v100, v180, v182
	v_cvt_pk_bf16_f32 v103, v64, v65
	v_cvt_pk_bf16_f32 v104, v66, v67
	s_lshl_b32 s31, s29, 14
	v_add_u32_e32 v182, s31, v253
	ds_read_b64_tr_b16 v[64:65], v182 offset:0
	ds_read_b64_tr_b16 v[66:67], v182 offset:0x100
	v_add_f32_e32 v68, v105, v68
	v_add_f32_e32 v68, v106, v68
	v_add_f32_e32 v68, v107, v68
	v_add_f32_e32 v68, v72, v68
	v_add_f32_e32 v68, v73, v68
	v_add_f32_e32 v215, v74, v68
	ds_read_b64_tr_b16 v[68:69], v182 offset:0x1000
	ds_read_b64_tr_b16 v[70:71], v182 offset:0x1100
	v_cvt_pk_bf16_f32 v108, v173, v175
	v_cvt_pk_bf16_f32 v109, v171, v174
	v_cvt_pk_bf16_f32 v110, v169, v172
	v_cvt_pk_bf16_f32 v111, v168, v170
	v_cvt_pk_bf16_f32 v101, v217, v218
	v_cvt_pk_bf16_f32 v102, v223, v232
	v_cvt_pk_bf16_f32 v105, v105, v106
	v_cvt_pk_bf16_f32 v106, v107, v72
	v_cvt_pk_bf16_f32 v107, v73, v74
	ds_read_b64_tr_b16 v[72:73], v182 offset:0x2000
	ds_read_b64_tr_b16 v[74:75], v182 offset:0x2100
	ds_read_b64_tr_b16 v[76:77], v182 offset:0x3000
	ds_read_b64_tr_b16 v[78:79], v182 offset:0x3100
	s_addc_u32 s67, s35, 0
	s_andn2_b64 vcc, exec, s[2:3]
	s_cbranch_vccnz .LBB4_777
	s_mov_b64 s[2:3], s[8:9]
	global_store_dwordx2 v193, v[184:185], s[2:3] nt
.LBB4_777:
	s_waitcnt lgkmcnt(0)
	v_mfma_f32_32x32x16_bf16 v[48:63], v[64:67], v[96:99], v[48:63]
	v_max_f32_e32 v64, v128, v129
	v_max3_f32 v64, v64, v130, v131
	v_max3_f32 v64, v64, v132, v133
	v_max3_f32 v64, v64, v134, v135
	v_max3_f32 v64, v64, v136, v137
	v_mfma_f32_32x32x16_bf16 v[48:63], v[68:71], v[108:111], v[48:63]
	v_max3_f32 v64, v64, v138, v139
	v_max3_f32 v66, v64, v140, v141
	ds_read_b64_tr_b16 v[64:65], v182 offset:0x200
	v_max3_f32 v180, v66, v142, v143
	ds_read_b64_tr_b16 v[66:67], v182 offset:0x300
	ds_read_b64_tr_b16 v[68:69], v182 offset:0x1200
	ds_read_b64_tr_b16 v[70:71], v182 offset:0x1300
	v_mfma_f32_32x32x16_bf16 v[48:63], v[72:75], v[100:103], v[48:63]
	ds_read_b64_tr_b16 v[72:73], v182 offset:0x2200
	ds_read_b64_tr_b16 v[74:75], v182 offset:0x2300
	ds_read_b64_tr_b16 v[218:219], v182 offset:0x3200
	ds_read_b64_tr_b16 v[220:221], v182 offset:0x3300
	v_mfma_f32_32x32x16_bf16 v[48:63], v[76:79], v[104:107], v[48:63]
	s_waitcnt lgkmcnt(0)
	v_mfma_f32_32x32x16_bf16 v[32:47], v[64:67], v[96:99], v[32:47]
	v_max3_f32 v76, v180, v112, v113
	v_max3_f32 v64, v76, v114, v115
	ds_read_b64_tr_b16 v[66:67], v182 offset:0x400
	v_max3_f32 v64, v64, v116, v117
	v_max3_f32 v64, v64, v118, v119
	v_max3_f32 v64, v64, v120, v121
	v_max3_f32 v64, v64, v122, v123
	v_mfma_f32_32x32x16_bf16 v[32:47], v[68:71], v[108:111], v[32:47]
	ds_read_b64_tr_b16 v[68:69], v182 offset:0x500
	ds_read_b64_tr_b16 v[70:71], v182 offset:0x1400
	v_max3_f32 v64, v64, v124, v125
	v_max3_f32 v64, v64, v126, v127
	v_mov_b32_e32 v65, v64
	s_nop 1
	v_permlane32_swap_b32_e32 v64, v65
	v_mfma_f32_32x32x16_bf16 v[32:47], v[72:75], v[100:103], v[32:47]
	ds_read_b64_tr_b16 v[72:73], v182 offset:0x1500
	ds_read_b64_tr_b16 v[74:75], v182 offset:0x2400
	ds_read_b64_tr_b16 v[76:77], v182 offset:0x2500
	ds_read_b64_tr_b16 v[222:223], v182 offset:0x3400
	ds_read_b64_tr_b16 v[224:225], v182 offset:0x3500
	v_mfma_f32_32x32x16_bf16 v[32:47], v[218:221], v[104:107], v[32:47]
	s_waitcnt lgkmcnt(0)
	v_max_f32_e32 v64, v64, v65
	v_mfma_f32_32x32x16_bf16 v[16:31], v[66:69], v[96:99], v[16:31]
	v_cmp_ge_f32_e32 vcc, s26, v64
	s_cmp_eq_u64 vcc, exec
	v_mfma_f32_32x32x16_bf16 v[16:31], v[70:73], v[108:111], v[16:31]
	v_mfma_f32_32x32x16_bf16 v[16:31], v[74:77], v[100:103], v[16:31]
	v_mfma_f32_32x32x16_bf16 v[16:31], v[222:225], v[104:107], v[16:31]
	s_cbranch_scc0 .LBB4_810
	v_mov_b32_e32 v180, 1.0

; #define AT_SBAR() __builtin_amdgcn_sched_barrier(0)
; template <int OFF> DI s16x4 tr_read(int vb) { s16x4 r; asm volatile("ds_read_b64_tr_b16 %0, %1 offset:%2" : "=&v"(r) : "v"(vb), "i"(OFF) : "memory"); return r; }
; DI void finishSM(f32x16& p0, f32x16& p1, float alpha, float& l_reg, bf16x8& pa0, bf16x8& pa1, bf16x8& pa2, bf16x8& pa3) {
; #pragma unroll
;     for (int r = 0; r < 16; ++r) p1[r] = __builtin_amdgcn_exp2f(p1[r]);
;     float ps = 0;
; #pragma unroll
;     for (int r = 0; r < 16; ++r) ps += p0[r];
; #pragma unroll
;     for (int r = 0; r < 16; ++r) ps += p1[r];
;     { auto rr = __builtin_amdgcn_permlane32_swap(__float_as_uint(ps), __float_as_uint(ps), false, false); ps = __uint_as_float(rr[0]) + __uint_as_float(rr[1]); }
;     l_reg = l_reg * alpha + ps;
;     ...
;     AT_PK4(p0, 0, pa0); AT_PK4(p0, 8, pa1); AT_PK4(p1, 0, pa2); AT_PK4(p1, 8, pa3);
;     ...
; }
; DI void qkt(f32x16& p0, f32x16& p1, const char* Ks, const bf16x8* qr, const f32x16& negm, int r32, int hi) {
; #pragma unroll
;     for (int d0 = 0; d0 < 4; ++d0) { const int cb = (d0 * 16 + hi * 8) * 2;
;         const bf16x8 b0 = *reinterpret_cast<const bf16x8*>(Ks + AT_KSWZ(r32, cb));
;         const bf16x8 b1 = *reinterpret_cast<const bf16x8*>(Ks + AT_KSWZ(32 + r32, cb));
;         p0 = __builtin_amdgcn_mfma_f32_32x32x16_bf16(b0, qr[d0], d0 == 0 ? negm : p0, 0, 0, 0);
;         p1 = __builtin_amdgcn_mfma_f32_32x32x16_bf16(b1, qr[d0], d0 == 0 ? negm : p1, 0, 0, 0); }
; }
; template <int D0> DI void pv_one(f32x16& od, int vb, bf16x8 pa0, bf16x8 pa1, bf16x8 pa2, bf16x8 pa3) {
;     const s16x4 l0 = tr_read<v_rd_off(D0, 0, 0)>(vb), h0 = tr_read<v_rd_off(D0, 0, 1)>(vb), l1 = tr_read<v_rd_off(D0, 1, 0)>(vb), h1 = tr_read<v_rd_off(D0, 1, 1)>(vb);
;     const s16x4 l2 = tr_read<v_rd_off(D0, 2, 0)>(vb), h2 = tr_read<v_rd_off(D0, 2, 1)>(vb), l3 = tr_read<v_rd_off(D0, 3, 0)>(vb), h3 = tr_read<v_rd_off(D0, 3, 1)>(vb);
;     asm volatile("s_waitcnt lgkmcnt(0)" ::: "memory"); AT_SBAR();
;     ...
;     od = __builtin_amdgcn_mfma_f32_32x32x16_bf16(AT_PK(l0, h0), pa0, od, 0, 0, 0);
;     od = __builtin_amdgcn_mfma_f32_32x32x16_bf16(AT_PK(l1, h1), pa1, od, 0, 0, 0);
;     od = __builtin_amdgcn_mfma_f32_32x32x16_bf16(AT_PK(l2, h2), pa2, od, 0, 0, 0);
;     od = __builtin_amdgcn_mfma_f32_32x32x16_bf16(AT_PK(l3, h3), pa3, od, 0, 0, 0);
;     ...
; }
.LBB4_796:
	v_exp_f32_e32 v182, v128
	v_exp_f32_e32 v234, v129
	v_exp_f32_e32 v235, v130
	v_exp_f32_e32 v236, v131
	v_exp_f32_e32 v237, v132
	v_exp_f32_e32 v238, v133
	v_exp_f32_e32 v239, v134
	v_exp_f32_e32 v240, v135
	v_exp_f32_e32 v241, v136
	v_exp_f32_e32 v242, v137
	v_exp_f32_e32 v243, v138
	v_exp_f32_e32 v244, v139
	v_exp_f32_e32 v245, v140
	v_exp_f32_e32 v246, v141
	v_exp_f32_e32 v247, v142
	v_exp_f32_e32 v248, v143
	v_add_u32_e32 v101, s65, v208
	v_add_u32_e32 v102, s65, v209
	v_add_u32_e32 v103, s65, v210
	ds_read_b128 v[172:175], v101 offset:49152
	ds_read_b128 v[176:179], v101 offset:53248
	ds_read_b128 v[218:221], v102 offset:49152
	ds_read_b128 v[222:225], v102 offset:53248
	ds_read_b128 v[226:229], v103 offset:49152
	ds_read_b128 v[230:233], v103 offset:53248
	v_exp_f32_e32 v112, v112
	v_exp_f32_e32 v113, v113
	v_exp_f32_e32 v114, v114
	s_waitcnt lgkmcnt(7)
	v_mfma_f32_32x32x16_bf16 v[128:143], v[96:99], v[156:159], v[80:95]
	s_add_u32 s24, s34, 0x2380c000
	s_addc_u32 s25, s35, 0
	s_add_u32 s34, s34, 0x2380e000
	s_addc_u32 s35, s35, 0
	s_add_u32 s66, s37, 0x21886000
	s_addc_u32 s67, s64, 0
	s_lshl_b32 s92, s29, 14
	s_add_i32 s92, s92, s94
	s_mov_b32 m0, s92
	s_lshl_b32 s96, s29, 13
	global_load_lds_dwordx4 v249, s[24:25]
	s_addk_i32 s92, 0x400
	s_mov_b32 m0, s92
	s_add_i32 s96, s96, s95
	global_load_lds_dwordx4 v250, s[24:25]
	s_nop 0
	s_mov_b32 m0, s96
	s_nop 0
	global_load_lds_dwordx4 v251, s[66:67]
	s_nop 0
	v_exp_f32_e32 v115, v115
	v_exp_f32_e32 v116, v116
	v_exp_f32_e32 v117, v117
	v_exp_f32_e32 v118, v118
	v_exp_f32_e32 v119, v119
	s_waitcnt lgkmcnt(6)
	v_mfma_f32_32x32x16_bf16 v[96:111], v[168:171], v[156:159], v[80:95]
	v_exp_f32_e32 v168, v120
	v_add_f32_e32 v120, 0, v182
	v_add_f32_e32 v120, v234, v120
	v_add_f32_e32 v120, v235, v120
	v_add_f32_e32 v120, v236, v120
	v_add_f32_e32 v120, v237, v120
	v_add_f32_e32 v120, v238, v120
	v_add_f32_e32 v120, v239, v120
	v_add_f32_e32 v120, v240, v120
	v_add_f32_e32 v120, v241, v120
	v_add_f32_e32 v120, v242, v120
	s_waitcnt lgkmcnt(5)
	v_mfma_f32_32x32x16_bf16 v[128:143], v[172:175], v[152:155], v[128:143]
	v_add_f32_e32 v120, v243, v120
	v_add_f32_e32 v120, v244, v120
	v_add_f32_e32 v120, v245, v120
	v_add_f32_e32 v120, v246, v120
	v_add_f32_e32 v120, v247, v120
	v_add_f32_e32 v120, v248, v120
	v_add_f32_e32 v120, v112, v120
	s_waitcnt lgkmcnt(4)
	v_mfma_f32_32x32x16_bf16 v[96:111], v[176:179], v[152:155], v[96:111]
	v_add_f32_e32 v120, v113, v120
	v_add_f32_e32 v120, v114, v120
	v_add_f32_e32 v120, v115, v120
	v_add_f32_e32 v120, v116, v120
	v_exp_f32_e32 v169, v121
	v_add_f32_e32 v120, v117, v120
	v_exp_f32_e32 v170, v122
	s_waitcnt lgkmcnt(3)
	v_mfma_f32_32x32x16_bf16 v[128:143], v[218:221], v[148:151], v[128:143]
	v_add_f32_e32 v120, v118, v120
	v_exp_f32_e32 v171, v123
	v_add_f32_e32 v120, v119, v120
	v_exp_f32_e32 v172, v124
	v_add_f32_e32 v120, v168, v120
	v_exp_f32_e32 v173, v125
	v_add_f32_e32 v120, v169, v120
	s_waitcnt lgkmcnt(2)
	v_mfma_f32_32x32x16_bf16 v[96:111], v[222:225], v[148:151], v[96:111]
	v_exp_f32_e32 v174, v126
	v_add_f32_e32 v120, v170, v120
	v_exp_f32_e32 v175, v127
	v_add_f32_e32 v120, v171, v120
	v_add_f32_e32 v120, v172, v120
	v_add_f32_e32 v120, v173, v120
	v_add_f32_e32 v120, v174, v120
	s_waitcnt lgkmcnt(1)
	v_mfma_f32_32x32x16_bf16 v[128:143], v[226:229], v[144:147], v[128:143]
	v_add_f32_e32 v217, v175, v120
	v_cvt_pk_bf16_f32 v120, v182, v234
	v_cvt_pk_bf16_f32 v121, v235, v236
	v_cvt_pk_bf16_f32 v122, v237, v238
	v_cvt_pk_bf16_f32 v123, v239, v240
	v_cvt_pk_bf16_f32 v124, v241, v242
	s_waitcnt lgkmcnt(0)
	v_mfma_f32_32x32x16_bf16 v[96:111], v[230:233], v[144:147], v[96:111]
	v_lshl_add_u32 v219, s30, 14, v253
	ds_read_b64_tr_b16 v[220:221], v219 offset:0
	ds_read_b64_tr_b16 v[222:223], v219 offset:0x100
	ds_read_b64_tr_b16 v[224:225], v219 offset:0x1000
	ds_read_b64_tr_b16 v[226:227], v219 offset:0x1100
	ds_read_b64_tr_b16 v[228:229], v219 offset:0x2000
	ds_read_b64_tr_b16 v[230:231], v219 offset:0x2100
	ds_read_b64_tr_b16 v[232:233], v219 offset:0x3000
	ds_read_b64_tr_b16 v[234:235], v219 offset:0x3100
	v_cvt_pk_bf16_f32 v125, v243, v244
	v_cvt_pk_bf16_f32 v126, v245, v246
	v_cvt_pk_bf16_f32 v127, v247, v248
	v_cvt_pk_bf16_f32 v112, v112, v113
	v_cvt_pk_bf16_f32 v113, v114, v115
	v_cvt_pk_bf16_f32 v114, v116, v117
	v_cvt_pk_bf16_f32 v115, v118, v119
	v_cvt_pk_bf16_f32 v116, v168, v169
	v_cvt_pk_bf16_f32 v117, v170, v171
	v_cvt_pk_bf16_f32 v118, v172, v173
	v_cvt_pk_bf16_f32 v119, v174, v175
	s_and_b64 vcc, exec, s[2:3]
	s_cbranch_vccnz .LBB4_798
	s_mov_b64 s[2:3], s[8:9]
	global_store_dwordx2 v193, v[184:185], s[2:3] nt
; #define AT_SBAR() __builtin_amdgcn_sched_barrier(0)
; template <int OFF> DI s16x4 tr_read(int vb) { s16x4 r; asm volatile("ds_read_b64_tr_b16 %0, %1 offset:%2" : "=&v"(r) : "v"(vb), "i"(OFF) : "memory"); return r; }
; template <int D0> DI void pv_one(f32x16& od, int vb, bf16x8 pa0, bf16x8 pa1, bf16x8 pa2, bf16x8 pa3) {
;     const s16x4 l0 = tr_read<v_rd_off(D0, 0, 0)>(vb), h0 = tr_read<v_rd_off(D0, 0, 1)>(vb), l1 = tr_read<v_rd_off(D0, 1, 0)>(vb), h1 = tr_read<v_rd_off(D0, 1, 1)>(vb);
;     const s16x4 l2 = tr_read<v_rd_off(D0, 2, 0)>(vb), h2 = tr_read<v_rd_off(D0, 2, 1)>(vb), l3 = tr_read<v_rd_off(D0, 3, 0)>(vb), h3 = tr_read<v_rd_off(D0, 3, 1)>(vb);
;     asm volatile("s_waitcnt lgkmcnt(0)" ::: "memory"); AT_SBAR();
;     ...
;     od = __builtin_amdgcn_mfma_f32_32x32x16_bf16(AT_PK(l0, h0), pa0, od, 0, 0, 0);
;     od = __builtin_amdgcn_mfma_f32_32x32x16_bf16(AT_PK(l1, h1), pa1, od, 0, 0, 0);
;     od = __builtin_amdgcn_mfma_f32_32x32x16_bf16(AT_PK(l2, h2), pa2, od, 0, 0, 0);
;     od = __builtin_amdgcn_mfma_f32_32x32x16_bf16(AT_PK(l3, h3), pa3, od, 0, 0, 0);
;     ...
; }
; DI void pv_all_sm(f32x16* o, int vb, bf16x8 pa0, bf16x8 pa1, bf16x8 pa2, bf16x8 pa3, f32x16& p0, f32x16& p1, float& m_ref, f32x16& negm, float& alpha) {
;     pv_one<0>(o[0], vb, pa0, pa1, pa2, pa3);
;     float pmax = p0[0];
; #pragma unroll
;     for (int r = 1; r < 16; ++r) pmax = fmaxf(pmax, p0[r]);
;     pv_one<1>(o[1], vb, pa0, pa1, pa2, pa3);
; #pragma unroll
;     for (int r = 0; r < 16; ++r) pmax = fmaxf(pmax, p1[r]);
;     { auto rr = __builtin_amdgcn_permlane32_swap(__float_as_uint(pmax), __float_as_uint(pmax), false, false); pmax = fmaxf(__uint_as_float(rr[0]), __uint_as_float(rr[1])); }
;     pv_one<2>(o[2], vb, pa0, pa1, pa2, pa3);
;     alpha = 1.f;
;     if (__builtin_expect(!__all(pmax <= THRL), 0)) {
;         const float dl = fmaxf(pmax, 0.f); m_ref += dl; alpha = __builtin_amdgcn_exp2f(-dl);
; #pragma unroll
;         for (int r = 0; r < 16; ++r) { p0[r] -= dl; p1[r] -= dl; }
; #pragma unroll
;         for (int r = 0; r < 16; ++r) negm[r] = -m_ref;
;     }
;     pv_one<3>(o[3], vb, pa0, pa1, pa2, pa3);
; #pragma unroll
;     for (int r = 0; r < 16; ++r) p0[r] = __builtin_amdgcn_exp2f(p0[r]);
; }
.LBB4_798:
	s_waitcnt lgkmcnt(0)
	v_mfma_f32_32x32x16_bf16 v[48:63], v[220:223], v[120:123], v[48:63]
	v_max_f32_e32 v182, v128, v129
	ds_read_b64_tr_b16 v[220:221], v219 offset:0x200
	ds_read_b64_tr_b16 v[222:223], v219 offset:0x300
	v_max3_f32 v182, v182, v130, v131
	v_max3_f32 v182, v182, v132, v133
	v_mfma_f32_32x32x16_bf16 v[48:63], v[224:227], v[124:127], v[48:63]
	ds_read_b64_tr_b16 v[224:225], v219 offset:0x1200
	ds_read_b64_tr_b16 v[226:227], v219 offset:0x1300
	v_max3_f32 v182, v182, v134, v135
	v_max3_f32 v182, v182, v136, v137
	v_max3_f32 v182, v182, v138, v139
	v_max3_f32 v182, v182, v140, v141
	v_max3_f32 v182, v182, v142, v143
	v_mfma_f32_32x32x16_bf16 v[48:63], v[228:231], v[112:115], v[48:63]
	ds_read_b64_tr_b16 v[228:229], v219 offset:0x2200
	ds_read_b64_tr_b16 v[230:231], v219 offset:0x2300
	ds_read_b64_tr_b16 v[236:237], v219 offset:0x3200
	ds_read_b64_tr_b16 v[238:239], v219 offset:0x3300
	v_mfma_f32_32x32x16_bf16 v[48:63], v[232:235], v[116:119], v[48:63]
	s_waitcnt lgkmcnt(0)
	v_mfma_f32_32x32x16_bf16 v[32:47], v[220:223], v[120:123], v[32:47]
	v_max3_f32 v182, v182, v96, v97
	v_max3_f32 v182, v182, v98, v99
	ds_read_b64_tr_b16 v[222:223], v219 offset:0x400
	v_max3_f32 v182, v182, v100, v101
	v_max3_f32 v182, v182, v102, v103
	v_max3_f32 v182, v182, v104, v105
	v_max3_f32 v182, v182, v106, v107
	v_mfma_f32_32x32x16_bf16 v[32:47], v[224:227], v[124:127], v[32:47]
	ds_read_b64_tr_b16 v[224:225], v219 offset:0x500
	ds_read_b64_tr_b16 v[226:227], v219 offset:0x1400
	v_max3_f32 v182, v182, v108, v109
	v_max3_f32 v182, v182, v110, v111
	v_mov_b32_e32 v220, v182
	s_nop 1
	v_permlane32_swap_b32_e32 v182, v220
	v_mfma_f32_32x32x16_bf16 v[32:47], v[228:231], v[112:115], v[32:47]
	ds_read_b64_tr_b16 v[228:229], v219 offset:0x1500
	ds_read_b64_tr_b16 v[230:231], v219 offset:0x2400
	ds_read_b64_tr_b16 v[232:233], v219 offset:0x2500
	ds_read_b64_tr_b16 v[240:241], v219 offset:0x3400
	ds_read_b64_tr_b16 v[242:243], v219 offset:0x3500
	v_mfma_f32_32x32x16_bf16 v[32:47], v[236:239], v[116:119], v[32:47]
	s_waitcnt lgkmcnt(0)
	v_max_f32_e32 v220, v182, v220
	v_mfma_f32_32x32x16_bf16 v[16:31], v[222:225], v[120:123], v[16:31]
	v_cmp_ge_f32_e32 vcc, s26, v220
	s_cmp_eq_u64 vcc, exec
	v_mov_b32_e32 v182, 1.0
	v_mfma_f32_32x32x16_bf16 v[16:31], v[226:229], v[124:127], v[16:31]
	v_mfma_f32_32x32x16_bf16 v[16:31], v[230:233], v[112:115], v[16:31]
	v_mfma_f32_32x32x16_bf16 v[16:31], v[240:243], v[116:119], v[16:31]
	s_cbranch_scc0 .LBB4_811

; DI void finishSM(f32x16& p0, f32x16& p1, float alpha, float& l_reg, bf16x8& pa0, bf16x8& pa1, bf16x8& pa2, bf16x8& pa3) {
; #pragma unroll
;     for (int r = 0; r < 16; ++r) p1[r] = __builtin_amdgcn_exp2f(p1[r]);
;     float ps = 0;
; #pragma unroll
;     for (int r = 0; r < 16; ++r) ps += p0[r];
; #pragma unroll
;     for (int r = 0; r < 16; ++r) ps += p1[r];
;     { auto rr = __builtin_amdgcn_permlane32_swap(__float_as_uint(ps), __float_as_uint(ps), false, false); ps = __uint_as_float(rr[0]) + __uint_as_float(rr[1]); }
;     l_reg = l_reg * alpha + ps;
;     ...
;     AT_PK4(p0, 0, pa0); AT_PK4(p0, 8, pa1); AT_PK4(p1, 0, pa2); AT_PK4(p1, 8, pa3);
;     ...
; }
; DI void qkt(f32x16& p0, f32x16& p1, const char* Ks, const bf16x8* qr, const f32x16& negm, int r32, int hi) {
; #pragma unroll
;     for (int d0 = 0; d0 < 4; ++d0) { const int cb = (d0 * 16 + hi * 8) * 2;
;         const bf16x8 b0 = *reinterpret_cast<const bf16x8*>(Ks + AT_KSWZ(r32, cb));
;         const bf16x8 b1 = *reinterpret_cast<const bf16x8*>(Ks + AT_KSWZ(32 + r32, cb));
;         p0 = __builtin_amdgcn_mfma_f32_32x32x16_bf16(b0, qr[d0], d0 == 0 ? negm : p0, 0, 0, 0);
;         p1 = __builtin_amdgcn_mfma_f32_32x32x16_bf16(b1, qr[d0], d0 == 0 ? negm : p1, 0, 0, 0); }
; }
; template <int D0> DI void pv_one(f32x16& od, int vb, bf16x8 pa0, bf16x8 pa1, bf16x8 pa2, bf16x8 pa3) {
;     const s16x4 l0 = tr_read<v_rd_off(D0, 0, 0)>(vb), h0 = tr_read<v_rd_off(D0, 0, 1)>(vb), l1 = tr_read<v_rd_off(D0, 1, 0)>(vb), h1 = tr_read<v_rd_off(D0, 1, 1)>(vb);
;     const s16x4 l2 = tr_read<v_rd_off(D0, 2, 0)>(vb), h2 = tr_read<v_rd_off(D0, 2, 1)>(vb), l3 = tr_read<v_rd_off(D0, 3, 0)>(vb), h3 = tr_read<v_rd_off(D0, 3, 1)>(vb);
;     asm volatile("s_waitcnt lgkmcnt(0)" ::: "memory"); AT_SBAR();
;     ...
;     od = __builtin_amdgcn_mfma_f32_32x32x16_bf16(AT_PK(l0, h0), pa0, od, 0, 0, 0);
;     od = __builtin_amdgcn_mfma_f32_32x32x16_bf16(AT_PK(l1, h1), pa1, od, 0, 0, 0);
;     od = __builtin_amdgcn_mfma_f32_32x32x16_bf16(AT_PK(l2, h2), pa2, od, 0, 0, 0);
;     od = __builtin_amdgcn_mfma_f32_32x32x16_bf16(AT_PK(l3, h3), pa3, od, 0, 0, 0);
;     ...
; }
; DI void pv_all_sm(f32x16* o, int vb, bf16x8 pa0, bf16x8 pa1, bf16x8 pa2, bf16x8 pa3, f32x16& p0, f32x16& p1, float& m_ref, f32x16& negm, float& alpha) {
;     pv_one<0>(o[0], vb, pa0, pa1, pa2, pa3);
;     float pmax = p0[0];
; #pragma unroll
;     for (int r = 1; r < 16; ++r) pmax = fmaxf(pmax, p0[r]);
.LBB4_849:
	s_lshl_b32 s26, s64, 13
	s_add_i32 s26, s26, 0
	v_add_u32_e32 v72, s26, v204
	v_add_u32_e32 v112, s26, v205
	v_add_u32_e32 v180, s26, v206
	s_waitcnt lgkmcnt(1)
	v_mfma_f32_32x32x16_bf16 v[128:143], v[64:67], v[156:159], v[80:95]
	ds_read_b128 v[64:67], v72 offset:49152
	ds_read_b128 v[72:75], v72 offset:53248
	ds_read_b128 v[76:79], v112 offset:49152
	ds_read_b128 v[220:223], v112 offset:53248
	s_add_u32 s66, s46, s28
	s_addc_u32 s67, s47, s29
	s_add_u32 s34, s66, 0x23808000
	s_addc_u32 s35, s67, 0
	s_add_u32 s76, s66, 0x2380a000
	s_add_u32 s74, s46, s24
	s_addc_u32 s75, s47, s25
	s_add_u32 s78, s74, 0x21804000
	s_addc_u32 s79, s75, 0
	s_lshl_b32 s92, s57, 14
	s_add_i32 s92, s92, s94
	s_mov_b32 m0, s92
	s_lshl_b32 s96, s57, 13
	global_load_lds_dwordx4 v249, s[34:35]
	s_addk_i32 s92, 0x400
	s_mov_b32 m0, s92
	s_add_i32 s96, s96, s95
	global_load_lds_dwordx4 v250, s[34:35]
	s_nop 0
	s_mov_b32 m0, s96
	s_nop 0
	global_load_lds_dwordx4 v251, s[78:79]
	v_exp_f32_e32 v182, v97
	v_exp_f32_e32 v213, v98
	v_exp_f32_e32 v214, v99
	v_exp_f32_e32 v219, v100
	v_exp_f32_e32 v228, v101
	s_waitcnt lgkmcnt(4)
	v_mfma_f32_32x32x16_bf16 v[112:127], v[68:71], v[156:159], v[80:95]
	ds_read_b128 v[68:71], v180 offset:49152
	ds_read_b128 v[224:227], v180 offset:53248
	v_exp_f32_e32 v180, v96
	v_cvt_pk_bf16_f32 v96, v216, v218
	v_cvt_pk_bf16_f32 v97, v179, v217
	v_cvt_pk_bf16_f32 v98, v177, v215
	v_cvt_pk_bf16_f32 v99, v176, v178
	s_waitcnt lgkmcnt(4)
	v_mfma_f32_32x32x16_bf16 v[112:127], v[72:75], v[152:155], v[112:127]
	v_add_f32_e32 v75, 0, v216
	v_add_f32_e32 v75, v218, v75
	v_add_f32_e32 v75, v179, v75
	v_add_f32_e32 v75, v217, v75
	v_add_f32_e32 v75, v177, v75
	v_add_f32_e32 v75, v215, v75
	v_add_f32_e32 v75, v176, v75
	v_mfma_f32_32x32x16_bf16 v[128:143], v[64:67], v[152:155], v[128:143]
	v_add_f32_e32 v75, v178, v75
	v_add_f32_e32 v75, v173, v75
	v_add_f32_e32 v75, v175, v75
	v_add_f32_e32 v75, v171, v75
	v_add_f32_e32 v75, v174, v75
	v_add_f32_e32 v75, v169, v75
	v_add_f32_e32 v75, v172, v75
	s_waitcnt lgkmcnt(3)
	v_mfma_f32_32x32x16_bf16 v[128:143], v[76:79], v[148:151], v[128:143]
	v_add_f32_e32 v75, v168, v75
	v_add_f32_e32 v75, v170, v75
	v_add_f32_e32 v75, v180, v75
	v_add_f32_e32 v75, v182, v75
	v_exp_f32_e32 v64, v102
	v_exp_f32_e32 v65, v103
	v_exp_f32_e32 v66, v104
	s_waitcnt lgkmcnt(2)
	v_mfma_f32_32x32x16_bf16 v[112:127], v[220:223], v[148:151], v[112:127]
	v_exp_f32_e32 v67, v105
	v_exp_f32_e32 v105, v106
	v_exp_f32_e32 v106, v107
	v_exp_f32_e32 v107, v108
	v_exp_f32_e32 v72, v109
	v_exp_f32_e32 v73, v110
	v_exp_f32_e32 v74, v111
	s_waitcnt lgkmcnt(1)
	v_mfma_f32_32x32x16_bf16 v[128:143], v[68:71], v[144:147], v[128:143]
	v_add_f32_e32 v68, v213, v75
	v_add_f32_e32 v68, v214, v68
	v_add_f32_e32 v68, v219, v68
	v_add_f32_e32 v68, v228, v68
	v_add_f32_e32 v68, v64, v68
	v_add_f32_e32 v68, v65, v68
	v_add_f32_e32 v68, v66, v68
	v_add_f32_e32 v68, v67, v68
	s_waitcnt lgkmcnt(0)
	v_mfma_f32_32x32x16_bf16 v[112:127], v[224:227], v[144:147], v[112:127]
	v_cvt_pk_bf16_f32 v100, v180, v182
	v_cvt_pk_bf16_f32 v103, v64, v65
	v_cvt_pk_bf16_f32 v104, v66, v67
	s_lshl_b32 s65, s63, 14
	v_add_u32_e32 v182, s65, v253
	ds_read_b64_tr_b16 v[64:65], v182 offset:0
	ds_read_b64_tr_b16 v[66:67], v182 offset:0x100
	v_add_f32_e32 v68, v105, v68
	v_add_f32_e32 v68, v106, v68
	v_add_f32_e32 v68, v107, v68
	v_add_f32_e32 v68, v72, v68
	v_add_f32_e32 v68, v73, v68
	v_add_f32_e32 v211, v74, v68
	ds_read_b64_tr_b16 v[68:69], v182 offset:0x1000
	ds_read_b64_tr_b16 v[70:71], v182 offset:0x1100
	v_cvt_pk_bf16_f32 v108, v173, v175
	v_cvt_pk_bf16_f32 v109, v171, v174
	v_cvt_pk_bf16_f32 v110, v169, v172
	v_cvt_pk_bf16_f32 v111, v168, v170
	v_cvt_pk_bf16_f32 v101, v213, v214
	v_cvt_pk_bf16_f32 v102, v219, v228
	v_cvt_pk_bf16_f32 v105, v105, v106
	v_cvt_pk_bf16_f32 v106, v107, v72
	v_cvt_pk_bf16_f32 v107, v73, v74
	ds_read_b64_tr_b16 v[72:73], v182 offset:0x2000
	ds_read_b64_tr_b16 v[74:75], v182 offset:0x2100
	ds_read_b64_tr_b16 v[76:77], v182 offset:0x3000
	ds_read_b64_tr_b16 v[78:79], v182 offset:0x3100
	s_addc_u32 s77, s67, 0
	s_andn2_b64 vcc, exec, s[2:3]
	s_cbranch_vccnz .LBB4_851
	s_mov_b64 s[2:3], s[8:9]
	global_store_dwordx2 v188, v[184:185], s[2:3] nt
.LBB4_851:
	s_waitcnt lgkmcnt(0)
	v_mfma_f32_32x32x16_bf16 v[32:47], v[64:67], v[96:99], v[32:47]
	v_max_f32_e32 v64, v128, v129
	v_max3_f32 v64, v64, v130, v131
	v_max3_f32 v64, v64, v132, v133
	v_max3_f32 v64, v64, v134, v135
	v_max3_f32 v64, v64, v136, v137
	v_mfma_f32_32x32x16_bf16 v[32:47], v[68:71], v[108:111], v[32:47]
	v_max3_f32 v64, v64, v138, v139
	v_max3_f32 v66, v64, v140, v141
	ds_read_b64_tr_b16 v[64:65], v182 offset:0x200
	v_max3_f32 v180, v66, v142, v143
	ds_read_b64_tr_b16 v[66:67], v182 offset:0x300
	ds_read_b64_tr_b16 v[68:69], v182 offset:0x1200
	ds_read_b64_tr_b16 v[70:71], v182 offset:0x1300
	v_mfma_f32_32x32x16_bf16 v[32:47], v[72:75], v[100:103], v[32:47]
	ds_read_b64_tr_b16 v[72:73], v182 offset:0x2200
	ds_read_b64_tr_b16 v[74:75], v182 offset:0x2300
	ds_read_b64_tr_b16 v[214:215], v182 offset:0x3200
	ds_read_b64_tr_b16 v[216:217], v182 offset:0x3300
	v_mfma_f32_32x32x16_bf16 v[32:47], v[76:79], v[104:107], v[32:47]
	s_waitcnt lgkmcnt(0)
	v_mfma_f32_32x32x16_bf16 v[48:63], v[64:67], v[96:99], v[48:63]
	v_max3_f32 v76, v180, v112, v113
	v_max3_f32 v64, v76, v114, v115
	ds_read_b64_tr_b16 v[66:67], v182 offset:0x400
	v_max3_f32 v64, v64, v116, v117
	v_max3_f32 v64, v64, v118, v119
	v_max3_f32 v64, v64, v120, v121
	v_max3_f32 v64, v64, v122, v123
	v_mfma_f32_32x32x16_bf16 v[48:63], v[68:71], v[108:111], v[48:63]
	ds_read_b64_tr_b16 v[68:69], v182 offset:0x500
	ds_read_b64_tr_b16 v[70:71], v182 offset:0x1400
	v_max3_f32 v64, v64, v124, v125
	v_max3_f32 v64, v64, v126, v127
	v_mov_b32_e32 v65, v64
	s_nop 1
	v_permlane32_swap_b32_e32 v64, v65
	v_mfma_f32_32x32x16_bf16 v[48:63], v[72:75], v[100:103], v[48:63]
	ds_read_b64_tr_b16 v[72:73], v182 offset:0x1500
	ds_read_b64_tr_b16 v[74:75], v182 offset:0x2400
	ds_read_b64_tr_b16 v[76:77], v182 offset:0x2500
	ds_read_b64_tr_b16 v[218:219], v182 offset:0x3400
	ds_read_b64_tr_b16 v[220:221], v182 offset:0x3500
	v_mfma_f32_32x32x16_bf16 v[48:63], v[214:217], v[104:107], v[48:63]
	s_waitcnt lgkmcnt(0)
	v_max_f32_e32 v64, v64, v65
	v_mfma_f32_32x32x16_bf16 v[16:31], v[66:69], v[96:99], v[16:31]
	v_cmp_ge_f32_e32 vcc, s15, v64
	s_cmp_eq_u64 vcc, exec
	v_mfma_f32_32x32x16_bf16 v[16:31], v[70:73], v[108:111], v[16:31]
	v_mfma_f32_32x32x16_bf16 v[16:31], v[74:77], v[100:103], v[16:31]
	v_mfma_f32_32x32x16_bf16 v[16:31], v[218:221], v[104:107], v[16:31]
	s_cbranch_scc0 .LBB4_884
	v_mov_b32_e32 v180, 1.0

; #define AT_SBAR() __builtin_amdgcn_sched_barrier(0)
; template <int OFF> DI s16x4 tr_read(int vb) { s16x4 r; asm volatile("ds_read_b64_tr_b16 %0, %1 offset:%2" : "=&v"(r) : "v"(vb), "i"(OFF) : "memory"); return r; }
; DI void finishSM(f32x16& p0, f32x16& p1, float alpha, float& l_reg, bf16x8& pa0, bf16x8& pa1, bf16x8& pa2, bf16x8& pa3) {
; #pragma unroll
;     for (int r = 0; r < 16; ++r) p1[r] = __builtin_amdgcn_exp2f(p1[r]);
;     float ps = 0;
; #pragma unroll
;     for (int r = 0; r < 16; ++r) ps += p0[r];
; #pragma unroll
;     for (int r = 0; r < 16; ++r) ps += p1[r];
;     { auto rr = __builtin_amdgcn_permlane32_swap(__float_as_uint(ps), __float_as_uint(ps), false, false); ps = __uint_as_float(rr[0]) + __uint_as_float(rr[1]); }
;     l_reg = l_reg * alpha + ps;
;     ...
;     AT_PK4(p0, 0, pa0); AT_PK4(p0, 8, pa1); AT_PK4(p1, 0, pa2); AT_PK4(p1, 8, pa3);
;     ...
; }
; DI void qkt(f32x16& p0, f32x16& p1, const char* Ks, const bf16x8* qr, const f32x16& negm, int r32, int hi) {
; #pragma unroll
;     for (int d0 = 0; d0 < 4; ++d0) { const int cb = (d0 * 16 + hi * 8) * 2;
;         const bf16x8 b0 = *reinterpret_cast<const bf16x8*>(Ks + AT_KSWZ(r32, cb));
;         const bf16x8 b1 = *reinterpret_cast<const bf16x8*>(Ks + AT_KSWZ(32 + r32, cb));
;         p0 = __builtin_amdgcn_mfma_f32_32x32x16_bf16(b0, qr[d0], d0 == 0 ? negm : p0, 0, 0, 0);
;         p1 = __builtin_amdgcn_mfma_f32_32x32x16_bf16(b1, qr[d0], d0 == 0 ? negm : p1, 0, 0, 0); }
; }
; template <int D0> DI void pv_one(f32x16& od, int vb, bf16x8 pa0, bf16x8 pa1, bf16x8 pa2, bf16x8 pa3) {
;     const s16x4 l0 = tr_read<v_rd_off(D0, 0, 0)>(vb), h0 = tr_read<v_rd_off(D0, 0, 1)>(vb), l1 = tr_read<v_rd_off(D0, 1, 0)>(vb), h1 = tr_read<v_rd_off(D0, 1, 1)>(vb);
;     const s16x4 l2 = tr_read<v_rd_off(D0, 2, 0)>(vb), h2 = tr_read<v_rd_off(D0, 2, 1)>(vb), l3 = tr_read<v_rd_off(D0, 3, 0)>(vb), h3 = tr_read<v_rd_off(D0, 3, 1)>(vb);
;     asm volatile("s_waitcnt lgkmcnt(0)" ::: "memory"); AT_SBAR();
;     ...
;     od = __builtin_amdgcn_mfma_f32_32x32x16_bf16(AT_PK(l0, h0), pa0, od, 0, 0, 0);
;     od = __builtin_amdgcn_mfma_f32_32x32x16_bf16(AT_PK(l1, h1), pa1, od, 0, 0, 0);
;     od = __builtin_amdgcn_mfma_f32_32x32x16_bf16(AT_PK(l2, h2), pa2, od, 0, 0, 0);
;     od = __builtin_amdgcn_mfma_f32_32x32x16_bf16(AT_PK(l3, h3), pa3, od, 0, 0, 0);
;     ...
; }
.LBB4_870:
	v_exp_f32_e32 v182, v128
	v_exp_f32_e32 v230, v129
	v_exp_f32_e32 v231, v130
	v_exp_f32_e32 v232, v131
	v_exp_f32_e32 v233, v132
	v_exp_f32_e32 v234, v133
	v_exp_f32_e32 v235, v134
	v_exp_f32_e32 v236, v135
	v_exp_f32_e32 v237, v136
	v_exp_f32_e32 v238, v137
	v_exp_f32_e32 v239, v138
	v_exp_f32_e32 v240, v139
	v_exp_f32_e32 v241, v140
	v_exp_f32_e32 v242, v141
	v_exp_f32_e32 v243, v142
	v_exp_f32_e32 v244, v143
	v_add_u32_e32 v101, s76, v204
	v_add_u32_e32 v102, s76, v205
	v_add_u32_e32 v103, s76, v206
	ds_read_b128 v[172:175], v101 offset:49152
	ds_read_b128 v[176:179], v101 offset:53248
	ds_read_b128 v[214:217], v102 offset:49152
	ds_read_b128 v[218:221], v102 offset:53248
	ds_read_b128 v[222:225], v103 offset:49152
	ds_read_b128 v[226:229], v103 offset:53248
	v_exp_f32_e32 v112, v112
	v_exp_f32_e32 v113, v113
	v_exp_f32_e32 v114, v114
	s_waitcnt lgkmcnt(7)
	v_mfma_f32_32x32x16_bf16 v[128:143], v[96:99], v[156:159], v[80:95]
	s_add_u32 s34, s66, 0x2380c000
	s_addc_u32 s35, s67, 0
	s_add_u32 s66, s66, 0x2380e000
	s_addc_u32 s67, s67, 0
	s_add_u32 s74, s74, 0x21806000
	s_addc_u32 s75, s75, 0
	s_lshl_b32 s92, s63, 14
	s_add_i32 s92, s92, s94
	s_mov_b32 m0, s92
	s_lshl_b32 s96, s63, 13
	global_load_lds_dwordx4 v249, s[34:35]
	s_addk_i32 s92, 0x400
	s_mov_b32 m0, s92
	s_add_i32 s96, s96, s95
	global_load_lds_dwordx4 v250, s[34:35]
	s_nop 0
	s_mov_b32 m0, s96
	s_nop 0
	global_load_lds_dwordx4 v251, s[74:75]
	s_nop 0
	v_exp_f32_e32 v115, v115
	v_exp_f32_e32 v116, v116
	v_exp_f32_e32 v117, v117
	v_exp_f32_e32 v118, v118
	v_exp_f32_e32 v119, v119
	s_waitcnt lgkmcnt(6)
	v_mfma_f32_32x32x16_bf16 v[96:111], v[168:171], v[156:159], v[80:95]
	v_exp_f32_e32 v168, v120
	v_add_f32_e32 v120, 0, v182
	v_add_f32_e32 v120, v230, v120
	v_add_f32_e32 v120, v231, v120
	v_add_f32_e32 v120, v232, v120
	v_add_f32_e32 v120, v233, v120
	v_add_f32_e32 v120, v234, v120
	v_add_f32_e32 v120, v235, v120
	v_add_f32_e32 v120, v236, v120
	v_add_f32_e32 v120, v237, v120
	v_add_f32_e32 v120, v238, v120
	s_waitcnt lgkmcnt(5)
	v_mfma_f32_32x32x16_bf16 v[128:143], v[172:175], v[152:155], v[128:143]
	v_add_f32_e32 v120, v239, v120
	v_add_f32_e32 v120, v240, v120
	v_add_f32_e32 v120, v241, v120
	v_add_f32_e32 v120, v242, v120
	v_add_f32_e32 v120, v243, v120
	v_add_f32_e32 v120, v244, v120
	v_add_f32_e32 v120, v112, v120
	s_waitcnt lgkmcnt(4)
	v_mfma_f32_32x32x16_bf16 v[96:111], v[176:179], v[152:155], v[96:111]
	v_add_f32_e32 v120, v113, v120
	v_add_f32_e32 v120, v114, v120
	v_add_f32_e32 v120, v115, v120
	v_add_f32_e32 v120, v116, v120
	v_exp_f32_e32 v169, v121
	v_add_f32_e32 v120, v117, v120
	v_exp_f32_e32 v170, v122
	s_waitcnt lgkmcnt(3)
	v_mfma_f32_32x32x16_bf16 v[128:143], v[214:217], v[148:151], v[128:143]
	v_add_f32_e32 v120, v118, v120
	v_exp_f32_e32 v171, v123
	v_add_f32_e32 v120, v119, v120
	v_exp_f32_e32 v172, v124
	v_add_f32_e32 v120, v168, v120
	v_exp_f32_e32 v173, v125
	v_add_f32_e32 v120, v169, v120
	s_waitcnt lgkmcnt(2)
	v_mfma_f32_32x32x16_bf16 v[96:111], v[218:221], v[148:151], v[96:111]
	v_exp_f32_e32 v174, v126
	v_add_f32_e32 v120, v170, v120
	v_exp_f32_e32 v175, v127
	v_add_f32_e32 v120, v171, v120
	v_add_f32_e32 v120, v172, v120
	v_add_f32_e32 v120, v173, v120
	v_add_f32_e32 v120, v174, v120
	s_waitcnt lgkmcnt(1)
	v_mfma_f32_32x32x16_bf16 v[128:143], v[222:225], v[144:147], v[128:143]
	v_add_f32_e32 v213, v175, v120
	v_cvt_pk_bf16_f32 v120, v182, v230
	v_cvt_pk_bf16_f32 v121, v231, v232
	v_cvt_pk_bf16_f32 v122, v233, v234
	v_cvt_pk_bf16_f32 v123, v235, v236
	v_cvt_pk_bf16_f32 v124, v237, v238
	s_waitcnt lgkmcnt(0)
	v_mfma_f32_32x32x16_bf16 v[96:111], v[226:229], v[144:147], v[96:111]
	v_lshl_add_u32 v215, s64, 14, v253
	ds_read_b64_tr_b16 v[216:217], v215 offset:0
	ds_read_b64_tr_b16 v[218:219], v215 offset:0x100
	ds_read_b64_tr_b16 v[220:221], v215 offset:0x1000
	ds_read_b64_tr_b16 v[222:223], v215 offset:0x1100
	ds_read_b64_tr_b16 v[224:225], v215 offset:0x2000
	ds_read_b64_tr_b16 v[226:227], v215 offset:0x2100
	ds_read_b64_tr_b16 v[228:229], v215 offset:0x3000
	ds_read_b64_tr_b16 v[230:231], v215 offset:0x3100
	v_cvt_pk_bf16_f32 v125, v239, v240
	v_cvt_pk_bf16_f32 v126, v241, v242
	v_cvt_pk_bf16_f32 v127, v243, v244
	v_cvt_pk_bf16_f32 v112, v112, v113
	v_cvt_pk_bf16_f32 v113, v114, v115
	v_cvt_pk_bf16_f32 v114, v116, v117
	v_cvt_pk_bf16_f32 v115, v118, v119
	v_cvt_pk_bf16_f32 v116, v168, v169
	v_cvt_pk_bf16_f32 v117, v170, v171
	v_cvt_pk_bf16_f32 v118, v172, v173
	v_cvt_pk_bf16_f32 v119, v174, v175
	s_and_b64 vcc, exec, s[2:3]
	s_cbranch_vccnz .LBB4_872
	s_mov_b64 s[2:3], s[8:9]
	global_store_dwordx2 v188, v[184:185], s[2:3] nt
; #define AT_SBAR() __builtin_amdgcn_sched_barrier(0)
; template <int OFF> DI s16x4 tr_read(int vb) { s16x4 r; asm volatile("ds_read_b64_tr_b16 %0, %1 offset:%2" : "=&v"(r) : "v"(vb), "i"(OFF) : "memory"); return r; }
; template <int D0> DI void pv_one(f32x16& od, int vb, bf16x8 pa0, bf16x8 pa1, bf16x8 pa2, bf16x8 pa3) {
;     const s16x4 l0 = tr_read<v_rd_off(D0, 0, 0)>(vb), h0 = tr_read<v_rd_off(D0, 0, 1)>(vb), l1 = tr_read<v_rd_off(D0, 1, 0)>(vb), h1 = tr_read<v_rd_off(D0, 1, 1)>(vb);
;     const s16x4 l2 = tr_read<v_rd_off(D0, 2, 0)>(vb), h2 = tr_read<v_rd_off(D0, 2, 1)>(vb), l3 = tr_read<v_rd_off(D0, 3, 0)>(vb), h3 = tr_read<v_rd_off(D0, 3, 1)>(vb);
;     asm volatile("s_waitcnt lgkmcnt(0)" ::: "memory"); AT_SBAR();
;     ...
;     od = __builtin_amdgcn_mfma_f32_32x32x16_bf16(AT_PK(l0, h0), pa0, od, 0, 0, 0);
;     od = __builtin_amdgcn_mfma_f32_32x32x16_bf16(AT_PK(l1, h1), pa1, od, 0, 0, 0);
;     od = __builtin_amdgcn_mfma_f32_32x32x16_bf16(AT_PK(l2, h2), pa2, od, 0, 0, 0);
;     od = __builtin_amdgcn_mfma_f32_32x32x16_bf16(AT_PK(l3, h3), pa3, od, 0, 0, 0);
;     ...
; }
; DI void pv_all_sm(f32x16* o, int vb, bf16x8 pa0, bf16x8 pa1, bf16x8 pa2, bf16x8 pa3, f32x16& p0, f32x16& p1, float& m_ref, f32x16& negm, float& alpha) {
;     pv_one<0>(o[0], vb, pa0, pa1, pa2, pa3);
;     float pmax = p0[0];
; #pragma unroll
;     for (int r = 1; r < 16; ++r) pmax = fmaxf(pmax, p0[r]);
;     pv_one<1>(o[1], vb, pa0, pa1, pa2, pa3);
; #pragma unroll
;     for (int r = 0; r < 16; ++r) pmax = fmaxf(pmax, p1[r]);
;     { auto rr = __builtin_amdgcn_permlane32_swap(__float_as_uint(pmax), __float_as_uint(pmax), false, false); pmax = fmaxf(__uint_as_float(rr[0]), __uint_as_float(rr[1])); }
;     pv_one<2>(o[2], vb, pa0, pa1, pa2, pa3);
;     alpha = 1.f;
;     if (__builtin_expect(!__all(pmax <= THRL), 0)) {
;         const float dl = fmaxf(pmax, 0.f); m_ref += dl; alpha = __builtin_amdgcn_exp2f(-dl);
; #pragma unroll
;         for (int r = 0; r < 16; ++r) { p0[r] -= dl; p1[r] -= dl; }
; #pragma unroll
;         for (int r = 0; r < 16; ++r) negm[r] = -m_ref;
;     }
;     pv_one<3>(o[3], vb, pa0, pa1, pa2, pa3);
; #pragma unroll
;     for (int r = 0; r < 16; ++r) p0[r] = __builtin_amdgcn_exp2f(p0[r]);
; }
.LBB4_872:
	s_waitcnt lgkmcnt(0)
	v_mfma_f32_32x32x16_bf16 v[32:47], v[216:219], v[120:123], v[32:47]
	v_max_f32_e32 v182, v128, v129
	ds_read_b64_tr_b16 v[216:217], v215 offset:0x200
	ds_read_b64_tr_b16 v[218:219], v215 offset:0x300
	v_max3_f32 v182, v182, v130, v131
	v_max3_f32 v182, v182, v132, v133
	v_mfma_f32_32x32x16_bf16 v[32:47], v[220:223], v[124:127], v[32:47]
	ds_read_b64_tr_b16 v[220:221], v215 offset:0x1200
	ds_read_b64_tr_b16 v[222:223], v215 offset:0x1300
	v_max3_f32 v182, v182, v134, v135
	v_max3_f32 v182, v182, v136, v137
	v_max3_f32 v182, v182, v138, v139
	v_max3_f32 v182, v182, v140, v141
	v_max3_f32 v182, v182, v142, v143
	v_mfma_f32_32x32x16_bf16 v[32:47], v[224:227], v[112:115], v[32:47]
	ds_read_b64_tr_b16 v[224:225], v215 offset:0x2200
	ds_read_b64_tr_b16 v[226:227], v215 offset:0x2300
	ds_read_b64_tr_b16 v[232:233], v215 offset:0x3200
	ds_read_b64_tr_b16 v[234:235], v215 offset:0x3300
	v_mfma_f32_32x32x16_bf16 v[32:47], v[228:231], v[116:119], v[32:47]
	s_waitcnt lgkmcnt(0)
	v_mfma_f32_32x32x16_bf16 v[48:63], v[216:219], v[120:123], v[48:63]
	v_max3_f32 v182, v182, v96, v97
	v_max3_f32 v182, v182, v98, v99
	ds_read_b64_tr_b16 v[218:219], v215 offset:0x400
	v_max3_f32 v182, v182, v100, v101
	v_max3_f32 v182, v182, v102, v103
	v_max3_f32 v182, v182, v104, v105
	v_max3_f32 v182, v182, v106, v107
	v_mfma_f32_32x32x16_bf16 v[48:63], v[220:223], v[124:127], v[48:63]
	ds_read_b64_tr_b16 v[220:221], v215 offset:0x500
	ds_read_b64_tr_b16 v[222:223], v215 offset:0x1400
	v_max3_f32 v182, v182, v108, v109
	v_max3_f32 v182, v182, v110, v111
	v_mov_b32_e32 v216, v182
	s_nop 1
	v_permlane32_swap_b32_e32 v182, v216
	v_mfma_f32_32x32x16_bf16 v[48:63], v[224:227], v[112:115], v[48:63]
	ds_read_b64_tr_b16 v[224:225], v215 offset:0x1500
	ds_read_b64_tr_b16 v[226:227], v215 offset:0x2400
	ds_read_b64_tr_b16 v[228:229], v215 offset:0x2500
	ds_read_b64_tr_b16 v[236:237], v215 offset:0x3400
	ds_read_b64_tr_b16 v[238:239], v215 offset:0x3500
	v_mfma_f32_32x32x16_bf16 v[48:63], v[232:235], v[116:119], v[48:63]
	s_waitcnt lgkmcnt(0)
	v_max_f32_e32 v216, v182, v216
	v_mfma_f32_32x32x16_bf16 v[16:31], v[218:221], v[120:123], v[16:31]
	v_cmp_ge_f32_e32 vcc, s15, v216
	s_cmp_eq_u64 vcc, exec
	v_mov_b32_e32 v182, 1.0
	v_mfma_f32_32x32x16_bf16 v[16:31], v[222:225], v[124:127], v[16:31]
	v_mfma_f32_32x32x16_bf16 v[16:31], v[226:229], v[112:115], v[16:31]
	v_mfma_f32_32x32x16_bf16 v[16:31], v[236:239], v[116:119], v[16:31]
	s_cbranch_scc0 .LBB4_885

; #define AT_SBAR() __builtin_amdgcn_sched_barrier(0)
; template <int OFF> DI s16x4 tr_read(int vb) { s16x4 r; asm volatile("ds_read_b64_tr_b16 %0, %1 offset:%2" : "=&v"(r) : "v"(vb), "i"(OFF) : "memory"); return r; }
; DI void finishSM(f32x16& p0, f32x16& p1, float alpha, float& l_reg, bf16x8& pa0, bf16x8& pa1, bf16x8& pa2, bf16x8& pa3) {
; #pragma unroll
;     for (int r = 0; r < 16; ++r) p1[r] = __builtin_amdgcn_exp2f(p1[r]);
;     float ps = 0;
; #pragma unroll
;     for (int r = 0; r < 16; ++r) ps += p0[r];
; #pragma unroll
;     for (int r = 0; r < 16; ++r) ps += p1[r];
;     { auto rr = __builtin_amdgcn_permlane32_swap(__float_as_uint(ps), __float_as_uint(ps), false, false); ps = __uint_as_float(rr[0]) + __uint_as_float(rr[1]); }
;     l_reg = l_reg * alpha + ps;
;     ...
;     AT_PK4(p0, 0, pa0); AT_PK4(p0, 8, pa1); AT_PK4(p1, 0, pa2); AT_PK4(p1, 8, pa3);
;     ...
; }
; DI void qkt(f32x16& p0, f32x16& p1, const char* Ks, const bf16x8* qr, const f32x16& negm, int r32, int hi) {
; #pragma unroll
;     for (int d0 = 0; d0 < 4; ++d0) { const int cb = (d0 * 16 + hi * 8) * 2;
;         const bf16x8 b0 = *reinterpret_cast<const bf16x8*>(Ks + AT_KSWZ(r32, cb));
;         const bf16x8 b1 = *reinterpret_cast<const bf16x8*>(Ks + AT_KSWZ(32 + r32, cb));
;         p0 = __builtin_amdgcn_mfma_f32_32x32x16_bf16(b0, qr[d0], d0 == 0 ? negm : p0, 0, 0, 0);
;         p1 = __builtin_amdgcn_mfma_f32_32x32x16_bf16(b1, qr[d0], d0 == 0 ? negm : p1, 0, 0, 0); }
; }
; template <int D0> DI void pv_one(f32x16& od, int vb, bf16x8 pa0, bf16x8 pa1, bf16x8 pa2, bf16x8 pa3) {
;     const s16x4 l0 = tr_read<v_rd_off(D0, 0, 0)>(vb), h0 = tr_read<v_rd_off(D0, 0, 1)>(vb), l1 = tr_read<v_rd_off(D0, 1, 0)>(vb), h1 = tr_read<v_rd_off(D0, 1, 1)>(vb);
;     const s16x4 l2 = tr_read<v_rd_off(D0, 2, 0)>(vb), h2 = tr_read<v_rd_off(D0, 2, 1)>(vb), l3 = tr_read<v_rd_off(D0, 3, 0)>(vb), h3 = tr_read<v_rd_off(D0, 3, 1)>(vb);
;     asm volatile("s_waitcnt lgkmcnt(0)" ::: "memory"); AT_SBAR();
;     ...
;     od = __builtin_amdgcn_mfma_f32_32x32x16_bf16(AT_PK(l0, h0), pa0, od, 0, 0, 0);
;     od = __builtin_amdgcn_mfma_f32_32x32x16_bf16(AT_PK(l1, h1), pa1, od, 0, 0, 0);
;     od = __builtin_amdgcn_mfma_f32_32x32x16_bf16(AT_PK(l2, h2), pa2, od, 0, 0, 0);
;     od = __builtin_amdgcn_mfma_f32_32x32x16_bf16(AT_PK(l3, h3), pa3, od, 0, 0, 0);
;     ...
; }
.LBB4_923:
	s_lshl_b32 s18, s30, 13
	s_add_i32 s18, s18, 0
	v_add_u32_e32 v72, s18, v208
	v_add_u32_e32 v112, s18, v209
	v_add_u32_e32 v180, s18, v210
	s_waitcnt lgkmcnt(1)
	v_mfma_f32_32x32x16_bf16 v[128:143], v[64:67], v[156:159], v[80:95]
	ds_read_b128 v[64:67], v72 offset:49152
	ds_read_b128 v[72:75], v72 offset:53248
	ds_read_b128 v[76:79], v112 offset:49152
	ds_read_b128 v[224:227], v112 offset:53248
	s_add_u32 s34, s46, s16
	s_addc_u32 s35, s47, s17
	s_add_u32 s24, s34, 0x23808000
	s_addc_u32 s25, s35, 0
	s_add_u32 s54, s34, 0x2380a000
	s_add_u32 s42, s46, s20
	s_addc_u32 s43, s47, s21
	s_add_u32 s56, s42, 0x21884000
	s_addc_u32 s57, s43, 0
	s_lshl_b32 s92, s15, 14
	s_add_i32 s92, s92, s94
	s_mov_b32 m0, s92
	s_lshl_b32 s96, s15, 13
	global_load_lds_dwordx4 v249, s[24:25]
	s_addk_i32 s92, 0x400
	s_mov_b32 m0, s92
	s_add_i32 s96, s96, s95
	global_load_lds_dwordx4 v250, s[24:25]
	s_nop 0
	s_mov_b32 m0, s96
	s_nop 0
	global_load_lds_dwordx4 v251, s[56:57]
	v_exp_f32_e32 v182, v97
	v_exp_f32_e32 v217, v98
	v_exp_f32_e32 v218, v99
	v_exp_f32_e32 v223, v100
	v_exp_f32_e32 v232, v101
	s_waitcnt lgkmcnt(4)
	v_mfma_f32_32x32x16_bf16 v[112:127], v[68:71], v[156:159], v[80:95]
	ds_read_b128 v[68:71], v180 offset:49152
	ds_read_b128 v[228:231], v180 offset:53248
	v_exp_f32_e32 v180, v96
	v_cvt_pk_bf16_f32 v96, v220, v222
	v_cvt_pk_bf16_f32 v97, v179, v221
	v_cvt_pk_bf16_f32 v98, v177, v219
	v_cvt_pk_bf16_f32 v99, v176, v178
	s_waitcnt lgkmcnt(4)
	v_mfma_f32_32x32x16_bf16 v[112:127], v[72:75], v[152:155], v[112:127]
	v_add_f32_e32 v75, 0, v220
	v_add_f32_e32 v75, v222, v75
	v_add_f32_e32 v75, v179, v75
	v_add_f32_e32 v75, v221, v75
	v_add_f32_e32 v75, v177, v75
	v_add_f32_e32 v75, v219, v75
	v_add_f32_e32 v75, v176, v75
	v_mfma_f32_32x32x16_bf16 v[128:143], v[64:67], v[152:155], v[128:143]
	v_add_f32_e32 v75, v178, v75
	v_add_f32_e32 v75, v173, v75
	v_add_f32_e32 v75, v175, v75
	v_add_f32_e32 v75, v171, v75
	v_add_f32_e32 v75, v174, v75
	v_add_f32_e32 v75, v169, v75
	v_add_f32_e32 v75, v172, v75
	s_waitcnt lgkmcnt(3)
	v_mfma_f32_32x32x16_bf16 v[128:143], v[76:79], v[148:151], v[128:143]
	v_add_f32_e32 v75, v168, v75
	v_add_f32_e32 v75, v170, v75
	v_add_f32_e32 v75, v180, v75
	v_add_f32_e32 v75, v182, v75
	v_exp_f32_e32 v64, v102
	v_exp_f32_e32 v65, v103
	v_exp_f32_e32 v66, v104
	s_waitcnt lgkmcnt(2)
	v_mfma_f32_32x32x16_bf16 v[112:127], v[224:227], v[148:151], v[112:127]
	v_exp_f32_e32 v67, v105
	v_exp_f32_e32 v105, v106
	v_exp_f32_e32 v106, v107
	v_exp_f32_e32 v107, v108
	v_exp_f32_e32 v72, v109
	v_exp_f32_e32 v73, v110
	v_exp_f32_e32 v74, v111
	s_waitcnt lgkmcnt(1)
	v_mfma_f32_32x32x16_bf16 v[128:143], v[68:71], v[144:147], v[128:143]
	v_add_f32_e32 v68, v217, v75
	v_add_f32_e32 v68, v218, v68
	v_add_f32_e32 v68, v223, v68
	v_add_f32_e32 v68, v232, v68
	v_add_f32_e32 v68, v64, v68
	v_add_f32_e32 v68, v65, v68
	v_add_f32_e32 v68, v66, v68
	v_add_f32_e32 v68, v67, v68
	s_waitcnt lgkmcnt(0)
	v_mfma_f32_32x32x16_bf16 v[112:127], v[228:231], v[144:147], v[112:127]
	v_cvt_pk_bf16_f32 v100, v180, v182
	v_cvt_pk_bf16_f32 v103, v64, v65
	v_cvt_pk_bf16_f32 v104, v66, v67
	s_lshl_b32 s31, s29, 14
	v_add_u32_e32 v182, s31, v253
	ds_read_b64_tr_b16 v[64:65], v182 offset:0
	ds_read_b64_tr_b16 v[66:67], v182 offset:0x100
	v_add_f32_e32 v68, v105, v68
	v_add_f32_e32 v68, v106, v68
	v_add_f32_e32 v68, v107, v68
	v_add_f32_e32 v68, v72, v68
	v_add_f32_e32 v68, v73, v68
	v_add_f32_e32 v215, v74, v68
	ds_read_b64_tr_b16 v[68:69], v182 offset:0x1000
	ds_read_b64_tr_b16 v[70:71], v182 offset:0x1100
	v_cvt_pk_bf16_f32 v108, v173, v175
	v_cvt_pk_bf16_f32 v109, v171, v174
	v_cvt_pk_bf16_f32 v110, v169, v172
	v_cvt_pk_bf16_f32 v111, v168, v170
	v_cvt_pk_bf16_f32 v101, v217, v218
	v_cvt_pk_bf16_f32 v102, v223, v232
	v_cvt_pk_bf16_f32 v105, v105, v106
	v_cvt_pk_bf16_f32 v106, v107, v72
	v_cvt_pk_bf16_f32 v107, v73, v74
	ds_read_b64_tr_b16 v[72:73], v182 offset:0x2000
	ds_read_b64_tr_b16 v[74:75], v182 offset:0x2100
	ds_read_b64_tr_b16 v[76:77], v182 offset:0x3000
	ds_read_b64_tr_b16 v[78:79], v182 offset:0x3100
	s_addc_u32 s55, s35, 0
	s_andn2_b64 vcc, exec, s[2:3]
	s_cbranch_vccnz .LBB4_925
	s_mov_b64 s[2:3], s[8:9]
	global_store_dwordx2 v193, v[184:185], s[2:3] nt

; #define AT_SBAR() __builtin_amdgcn_sched_barrier(0)
; template <int OFF> DI s16x4 tr_read(int vb) { s16x4 r; asm volatile("ds_read_b64_tr_b16 %0, %1 offset:%2" : "=&v"(r) : "v"(vb), "i"(OFF) : "memory"); return r; }
; DI void finishSM(f32x16& p0, f32x16& p1, float alpha, float& l_reg, bf16x8& pa0, bf16x8& pa1, bf16x8& pa2, bf16x8& pa3) {
; #pragma unroll
;     for (int r = 0; r < 16; ++r) p1[r] = __builtin_amdgcn_exp2f(p1[r]);
;     float ps = 0;
; #pragma unroll
;     for (int r = 0; r < 16; ++r) ps += p0[r];
; #pragma unroll
;     for (int r = 0; r < 16; ++r) ps += p1[r];
;     { auto rr = __builtin_amdgcn_permlane32_swap(__float_as_uint(ps), __float_as_uint(ps), false, false); ps = __uint_as_float(rr[0]) + __uint_as_float(rr[1]); }
;     l_reg = l_reg * alpha + ps;
;     ...
;     AT_PK4(p0, 0, pa0); AT_PK4(p0, 8, pa1); AT_PK4(p1, 0, pa2); AT_PK4(p1, 8, pa3);
;     ...
; }
; DI void qkt(f32x16& p0, f32x16& p1, const char* Ks, const bf16x8* qr, const f32x16& negm, int r32, int hi) {
; #pragma unroll
;     for (int d0 = 0; d0 < 4; ++d0) { const int cb = (d0 * 16 + hi * 8) * 2;
;         const bf16x8 b0 = *reinterpret_cast<const bf16x8*>(Ks + AT_KSWZ(r32, cb));
;         const bf16x8 b1 = *reinterpret_cast<const bf16x8*>(Ks + AT_KSWZ(32 + r32, cb));
;         p0 = __builtin_amdgcn_mfma_f32_32x32x16_bf16(b0, qr[d0], d0 == 0 ? negm : p0, 0, 0, 0);
;         p1 = __builtin_amdgcn_mfma_f32_32x32x16_bf16(b1, qr[d0], d0 == 0 ? negm : p1, 0, 0, 0); }
; }
; template <int D0> DI void pv_one(f32x16& od, int vb, bf16x8 pa0, bf16x8 pa1, bf16x8 pa2, bf16x8 pa3) {
;     const s16x4 l0 = tr_read<v_rd_off(D0, 0, 0)>(vb), h0 = tr_read<v_rd_off(D0, 0, 1)>(vb), l1 = tr_read<v_rd_off(D0, 1, 0)>(vb), h1 = tr_read<v_rd_off(D0, 1, 1)>(vb);
;     const s16x4 l2 = tr_read<v_rd_off(D0, 2, 0)>(vb), h2 = tr_read<v_rd_off(D0, 2, 1)>(vb), l3 = tr_read<v_rd_off(D0, 3, 0)>(vb), h3 = tr_read<v_rd_off(D0, 3, 1)>(vb);
;     asm volatile("s_waitcnt lgkmcnt(0)" ::: "memory"); AT_SBAR();
;     ...
;     od = __builtin_amdgcn_mfma_f32_32x32x16_bf16(AT_PK(l0, h0), pa0, od, 0, 0, 0);
;     od = __builtin_amdgcn_mfma_f32_32x32x16_bf16(AT_PK(l1, h1), pa1, od, 0, 0, 0);
;     od = __builtin_amdgcn_mfma_f32_32x32x16_bf16(AT_PK(l2, h2), pa2, od, 0, 0, 0);
;     od = __builtin_amdgcn_mfma_f32_32x32x16_bf16(AT_PK(l3, h3), pa3, od, 0, 0, 0);
;     ...
; }
.LBB4_944:
	v_exp_f32_e32 v182, v128
	v_exp_f32_e32 v234, v129
	v_exp_f32_e32 v235, v130
	v_exp_f32_e32 v236, v131
	v_exp_f32_e32 v237, v132
	v_exp_f32_e32 v238, v133
	v_exp_f32_e32 v239, v134
	v_exp_f32_e32 v240, v135
	v_exp_f32_e32 v241, v136
	v_exp_f32_e32 v242, v137
	v_exp_f32_e32 v243, v138
	v_exp_f32_e32 v244, v139
	v_exp_f32_e32 v245, v140
	v_exp_f32_e32 v246, v141
	v_exp_f32_e32 v247, v142
	v_exp_f32_e32 v248, v143
	v_add_u32_e32 v101, s54, v208
	v_add_u32_e32 v102, s54, v209
	v_add_u32_e32 v103, s54, v210
	ds_read_b128 v[172:175], v101 offset:49152
	ds_read_b128 v[176:179], v101 offset:53248
	ds_read_b128 v[218:221], v102 offset:49152
	ds_read_b128 v[222:225], v102 offset:53248
	ds_read_b128 v[226:229], v103 offset:49152
	ds_read_b128 v[230:233], v103 offset:53248
	v_exp_f32_e32 v112, v112
	v_exp_f32_e32 v113, v113
	v_exp_f32_e32 v114, v114
	s_waitcnt lgkmcnt(7)
	v_mfma_f32_32x32x16_bf16 v[128:143], v[96:99], v[156:159], v[80:95]
	s_add_u32 s24, s34, 0x2380c000
	s_addc_u32 s25, s35, 0
	s_add_u32 s34, s34, 0x2380e000
	s_addc_u32 s35, s35, 0
	s_add_u32 s42, s42, 0x21886000
	s_addc_u32 s43, s43, 0
	s_lshl_b32 s92, s29, 14
	s_add_i32 s92, s92, s94
	s_mov_b32 m0, s92
	s_lshl_b32 s96, s29, 13
	global_load_lds_dwordx4 v249, s[24:25]
	s_addk_i32 s92, 0x400
	s_mov_b32 m0, s92
	s_add_i32 s96, s96, s95
	global_load_lds_dwordx4 v250, s[24:25]
	s_nop 0
	s_mov_b32 m0, s96
	s_nop 0
	global_load_lds_dwordx4 v251, s[42:43]
	s_nop 0
	v_exp_f32_e32 v115, v115
	v_exp_f32_e32 v116, v116
	v_exp_f32_e32 v117, v117
	v_exp_f32_e32 v118, v118
	v_exp_f32_e32 v119, v119
	s_waitcnt lgkmcnt(6)
	v_mfma_f32_32x32x16_bf16 v[96:111], v[168:171], v[156:159], v[80:95]
	v_exp_f32_e32 v168, v120
	v_add_f32_e32 v120, 0, v182
	v_add_f32_e32 v120, v234, v120
	v_add_f32_e32 v120, v235, v120
	v_add_f32_e32 v120, v236, v120
	v_add_f32_e32 v120, v237, v120
	v_add_f32_e32 v120, v238, v120
	v_add_f32_e32 v120, v239, v120
	v_add_f32_e32 v120, v240, v120
	v_add_f32_e32 v120, v241, v120
	v_add_f32_e32 v120, v242, v120
	s_waitcnt lgkmcnt(5)
	v_mfma_f32_32x32x16_bf16 v[128:143], v[172:175], v[152:155], v[128:143]
	v_add_f32_e32 v120, v243, v120
	v_add_f32_e32 v120, v244, v120
	v_add_f32_e32 v120, v245, v120
	v_add_f32_e32 v120, v246, v120
	v_add_f32_e32 v120, v247, v120
	v_add_f32_e32 v120, v248, v120
	v_add_f32_e32 v120, v112, v120
	s_waitcnt lgkmcnt(4)
	v_mfma_f32_32x32x16_bf16 v[96:111], v[176:179], v[152:155], v[96:111]
	v_add_f32_e32 v120, v113, v120
	v_add_f32_e32 v120, v114, v120
	v_add_f32_e32 v120, v115, v120
	v_add_f32_e32 v120, v116, v120
	v_exp_f32_e32 v169, v121
	v_add_f32_e32 v120, v117, v120
	v_exp_f32_e32 v170, v122
	s_waitcnt lgkmcnt(3)
	v_mfma_f32_32x32x16_bf16 v[128:143], v[218:221], v[148:151], v[128:143]
	v_add_f32_e32 v120, v118, v120
	v_exp_f32_e32 v171, v123
	v_add_f32_e32 v120, v119, v120
	v_exp_f32_e32 v172, v124
	v_add_f32_e32 v120, v168, v120
	v_exp_f32_e32 v173, v125
	v_add_f32_e32 v120, v169, v120
	s_waitcnt lgkmcnt(2)
	v_mfma_f32_32x32x16_bf16 v[96:111], v[222:225], v[148:151], v[96:111]
	v_exp_f32_e32 v174, v126
	v_add_f32_e32 v120, v170, v120
	v_exp_f32_e32 v175, v127
	v_add_f32_e32 v120, v171, v120
	v_add_f32_e32 v120, v172, v120
	v_add_f32_e32 v120, v173, v120
	v_add_f32_e32 v120, v174, v120
	s_waitcnt lgkmcnt(1)
	v_mfma_f32_32x32x16_bf16 v[128:143], v[226:229], v[144:147], v[128:143]
	v_add_f32_e32 v217, v175, v120
	v_cvt_pk_bf16_f32 v120, v182, v234
	v_cvt_pk_bf16_f32 v121, v235, v236
	v_cvt_pk_bf16_f32 v122, v237, v238
	v_cvt_pk_bf16_f32 v123, v239, v240
	v_cvt_pk_bf16_f32 v124, v241, v242
	s_waitcnt lgkmcnt(0)
	v_mfma_f32_32x32x16_bf16 v[96:111], v[230:233], v[144:147], v[96:111]
	v_lshl_add_u32 v219, s30, 14, v253
	ds_read_b64_tr_b16 v[220:221], v219 offset:0
	ds_read_b64_tr_b16 v[222:223], v219 offset:0x100
	ds_read_b64_tr_b16 v[224:225], v219 offset:0x1000
	ds_read_b64_tr_b16 v[226:227], v219 offset:0x1100
	ds_read_b64_tr_b16 v[228:229], v219 offset:0x2000
	ds_read_b64_tr_b16 v[230:231], v219 offset:0x2100
	ds_read_b64_tr_b16 v[232:233], v219 offset:0x3000
	ds_read_b64_tr_b16 v[234:235], v219 offset:0x3100
	v_cvt_pk_bf16_f32 v125, v243, v244
	v_cvt_pk_bf16_f32 v126, v245, v246
	v_cvt_pk_bf16_f32 v127, v247, v248
	v_cvt_pk_bf16_f32 v112, v112, v113
	v_cvt_pk_bf16_f32 v113, v114, v115
	v_cvt_pk_bf16_f32 v114, v116, v117
	v_cvt_pk_bf16_f32 v115, v118, v119
	v_cvt_pk_bf16_f32 v116, v168, v169
	v_cvt_pk_bf16_f32 v117, v170, v171
	v_cvt_pk_bf16_f32 v118, v172, v173
	v_cvt_pk_bf16_f32 v119, v174, v175
	s_and_b64 vcc, exec, s[2:3]
	s_cbranch_vccnz .LBB4_946
	s_mov_b64 s[2:3], s[8:9]
	global_store_dwordx2 v193, v[184:185], s[2:3] nt
